# speedup vs baseline: 1.0289x; 1.0289x over previous
_Z8gat_mainPKiPKDF16_PKfS4_Pf:
	s_load_dwordx8 s[24:31], s[0:1], 0x0
	s_load_dwordx2 s[12:13], s[0:1], 0x20
	v_and_b32_e32 v2, 63, v0
	v_readfirstlane_b32 s16, v0
	v_lshlrev_b32_e32 v1, 4, v2
	s_lshr_b32 s16, s16, 6
	s_and_b32 s17, s2, 7
	s_lshr_b32 s18, s2, 3
	s_lshr_b32 s19, s18, 3
	s_add_u32 s19, s19, s18
	s_and_b32 s19, s19, 7
	s_lshr_b32 s20, s16, 2
	s_and_b32 s21, s16, 3
	s_lshl_b32 s22, s16, 16
	s_lshl_b32 s23, s16, 12
	s_waitcnt lgkmcnt(0)
	s_lshl_b32 s3, s17, 24
	s_lshl_b32 s57, s18, 19
	s_add_u32 s3, s3, s57
	s_add_u32 s4, s24, s3
	s_addc_u32 s5, s25, 0
	s_and_b32 s5, s5, 0xffff
	s_mov_b32 s6, 0x80000
	s_mov_b32 s7, 0x20000
	s_lshl_b32 s3, s17, 18
	s_add_u32 s8, s26, s3
	s_addc_u32 s9, s27, 0
	s_and_b32 s9, s9, 0xffff
	s_mov_b32 s10, 0x40000
	s_mov_b32 s11, 0x20000
	s_lshl_b32 s3, s17, 11
	s_lshl_b32 s57, s18, 6
	s_add_u32 s3, s3, s57
	s_lshl_b32 s57, s16, 3
	s_add_u32 s3, s3, s57
	s_lshl_b32 s3, s3, 2
	s_add_u32 s28, s28, s3
	s_addc_u32 s29, s29, 0
	v_and_b32_e32 v36, 7, v0
	v_lshlrev_b32_e32 v36, 2, v36
	global_load_dword v37, v36, s[28:29]
	s_lshl_b32 s3, s17, 13
	s_add_u32 s30, s30, s3
	s_addc_u32 s31, s31, 0
	v_lshlrev_b32_e32 v38, 4, v0
	global_load_dwordx4 v[24:27], v38, s[30:31]
	s_add_u32 s3, s19, 0
	s_and_b32 s3, s3, 7
	s_lshl_b32 s57, s3, 10
	s_add_u32 s48, s57, s22
	s_add_u32 s49, s48, 0x2000
	s_add_u32 s50, s48, 0x4000
	s_add_u32 s51, s48, 0x6000
	s_add_u32 s52, s48, 0x8000
	s_add_u32 s53, s48, 0xa000
	s_add_u32 s54, s48, 0xc000
	s_add_u32 s55, s48, 0xe000
	s_lshl_b32 s56, s3, 15
	s_add_u32 s56, s56, s23
	buffer_load_dwordx4 v[88:91], v1, s[4:7], s48 offen nt
	buffer_load_dwordx4 v[92:95], v1, s[4:7], s49 offen nt
	buffer_load_dwordx4 v[96:99], v1, s[4:7], s50 offen nt
	buffer_load_dwordx4 v[100:103], v1, s[4:7], s51 offen nt
	buffer_load_dwordx4 v[104:107], v1, s[4:7], s52 offen nt
	buffer_load_dwordx4 v[108:111], v1, s[4:7], s53 offen nt
	buffer_load_dwordx4 v[112:115], v1, s[4:7], s54 offen nt
	buffer_load_dwordx4 v[116:119], v1, s[4:7], s55 offen nt
	buffer_load_dwordx4 v[152:155], v1, s[8:11], s56 offen
	buffer_load_dwordx4 v[156:159], v1, s[8:11], s56 offen offset:1024
	buffer_load_dwordx4 v[160:163], v1, s[8:11], s56 offen offset:2048
	buffer_load_dwordx4 v[164:167], v1, s[8:11], s56 offen offset:3072
	s_mul_i32 s3, s16, 0x1080
	v_lshlrev_b32_e32 v3, 3, v2
	v_add_u32_e32 v3, s3, v3
	v_add_u32_e32 v4, 0x840, v3
	v_add_u32_e32 v5, 0x8400, v3
	v_add_u32_e32 v6, 0x8400, v4
	v_and_b32_e32 v36, 31, v2
	v_mul_u32_u24_e32 v36, 0x210, v36
	v_lshrrev_b32_e32 v38, 5, v2
	v_lshlrev_b32_e32 v38, 4, v38
	v_add_u32_e32 v7, v36, v38
	s_mul_i32 s3, s20, 0x4200
	s_lshl_b32 s57, s21, 7
	s_add_u32 s3, s3, s57
	v_add_u32_e32 v7, s3, v7
	s_lshl_b32 s3, s21, 13
	s_add_u32 s3, s3, 0x14800
	v_add_u32_e32 v8, s3, v1
	s_add_u32 s3, s23, 0x14800
	v_add_u32_e32 v9, s3, v1
	v_add_u32_e32 v10, 0x10800, v1
	v_mov_b32_e32 v12, 0x3c003c00
	v_mov_b32_e32 v13, 0x3c003c00
	v_mov_b32_e32 v14, 0x3c003c00
	v_mov_b32_e32 v15, 0x3c003c00
	v_mov_b32_e32 v40, 0
	v_mov_b32_e32 v41, 0
	v_mov_b32_e32 v42, 0
	v_mov_b32_e32 v43, 0
	v_mov_b32_e32 v44, 0
	v_mov_b32_e32 v45, 0
	v_mov_b32_e32 v46, 0
	v_mov_b32_e32 v47, 0
	v_mov_b32_e32 v48, 0
	v_mov_b32_e32 v49, 0
	v_mov_b32_e32 v50, 0
	v_mov_b32_e32 v51, 0
	v_mov_b32_e32 v52, 0
	v_mov_b32_e32 v53, 0
	v_mov_b32_e32 v54, 0
	v_mov_b32_e32 v55, 0
	v_mov_b32_e32 v56, 0
	v_mov_b32_e32 v57, 0
	v_mov_b32_e32 v58, 0
	v_mov_b32_e32 v59, 0
	v_mov_b32_e32 v60, 0
	v_mov_b32_e32 v61, 0
	v_mov_b32_e32 v62, 0
	v_mov_b32_e32 v63, 0
	v_mov_b32_e32 v64, 0
	v_mov_b32_e32 v65, 0
	v_mov_b32_e32 v66, 0
	v_mov_b32_e32 v67, 0
	v_mov_b32_e32 v68, 0
	v_mov_b32_e32 v69, 0
	v_mov_b32_e32 v70, 0
	v_mov_b32_e32 v71, 0
	v_mov_b32_e32 v72, 0
	v_mov_b32_e32 v73, 0
	v_mov_b32_e32 v74, 0
	v_mov_b32_e32 v75, 0
	v_mov_b32_e32 v76, 0
	v_mov_b32_e32 v77, 0
	v_mov_b32_e32 v78, 0
	v_mov_b32_e32 v79, 0
	v_mov_b32_e32 v80, 0
	v_mov_b32_e32 v81, 0
	v_mov_b32_e32 v82, 0
	v_mov_b32_e32 v83, 0
	v_mov_b32_e32 v84, 0
	v_mov_b32_e32 v85, 0
	v_mov_b32_e32 v86, 0
	v_mov_b32_e32 v87, 0
	s_lshl_b32 s3, s17, 11
	s_lshl_b32 s57, s18, 6
	s_add_u32 s3, s3, s57
	s_lshl_b32 s57, s20, 5
	s_add_u32 s3, s3, s57
	s_lshl_b32 s57, s21, 3
	s_add_u32 s3, s3, s57
	s_lshl_b32 s3, s3, 8
	s_add_u32 s12, s12, s3
	s_addc_u32 s13, s13, 0
	s_waitcnt vmcnt(12)
	v_max_f32_e32 v28, v24, v25
	v_max3_f32 v28, v28, v26, v27
	v_lshlrev_b32_e32 v29, 2, v2
	v_xor_b32_e32 v30, 4, v29
	ds_bpermute_b32 v31, v30, v28
	s_waitcnt lgkmcnt(0)
	v_max_f32_e32 v28, v28, v31
	v_xor_b32_e32 v30, 8, v29
	ds_bpermute_b32 v31, v30, v28
	s_waitcnt lgkmcnt(0)
	v_max_f32_e32 v28, v28, v31
	v_xor_b32_e32 v30, 16, v29
	ds_bpermute_b32 v31, v30, v28
	s_waitcnt lgkmcnt(0)
	v_max_f32_e32 v28, v28, v31
	v_xor_b32_e32 v30, 32, v29
	ds_bpermute_b32 v31, v30, v28
	s_waitcnt lgkmcnt(0)
	v_max_f32_e32 v28, v28, v31
	v_xor_b32_e32 v30, 64, v29
	ds_bpermute_b32 v31, v30, v28
	s_waitcnt lgkmcnt(0)
	v_max_f32_e32 v28, v28, v31
	v_xor_b32_e32 v30, 128, v29
	ds_bpermute_b32 v31, v30, v28
	s_waitcnt lgkmcnt(0)
	v_max_f32_e32 v28, v28, v31
	s_lshl_b32 s3, s16, 2
	s_add_u32 s3, s3, 0x24800
	v_mov_b32_e32 v30, s3
	ds_write_b32 v30, v28
	s_waitcnt lgkmcnt(0)
	s_barrier
	v_mov_b32_e32 v30, 0x24800
	ds_read_b128 v[32:35], v30
	ds_read_b128 v[16:19], v30 offset:16
	s_waitcnt lgkmcnt(0)
	v_max3_f32 v28, v32, v33, v34
	v_max3_f32 v28, v28, v35, v16
	v_max3_f32 v28, v28, v17, v18
	v_max_f32_e32 v28, v28, v19
	v_sub_f32_e32 v16, v24, v28
	v_sub_f32_e32 v17, v25, v28
	v_sub_f32_e32 v18, v26, v28
	v_sub_f32_e32 v19, v27, v28
	v_mul_f32_e32 v20, 0x3e4ccccd, v16
	v_mul_f32_e32 v21, 0x3e4ccccd, v17
	v_mul_f32_e32 v22, 0x3e4ccccd, v18
	v_mul_f32_e32 v23, 0x3e4ccccd, v19
	v_exp_f32_e32 v16, v16
	v_exp_f32_e32 v17, v17
	v_exp_f32_e32 v18, v18
	v_exp_f32_e32 v19, v19
	v_exp_f32_e32 v20, v20
	v_exp_f32_e32 v21, v21
	v_exp_f32_e32 v22, v22
	v_exp_f32_e32 v23, v23
	v_lshlrev_b32_e32 v30, 4, v0
	v_add_u32_e32 v30, 0x10800, v30
	ds_write_b128 v30, v[16:19]
	ds_write_b128 v30, v[20:23] offset:8192
	v_add_f32_e32 v36, v37, v28
	v_mul_f32_e32 v38, 0x3e4ccccd, v36
	v_max_f32_e32 v39, v36, v38
	v_sub_f32_e32 v36, v36, v39
	v_sub_f32_e32 v38, v38, v39
	v_add_f32_e32 v36, 0x41600000, v36
	v_add_f32_e32 v38, 0x41600000, v38
	v_exp_f32_e32 v36, v36
	v_exp_f32_e32 v38, v38
	s_nop 1
	v_readlane_b32 s32, v36, 0
	v_readlane_b32 s33, v36, 1
	v_readlane_b32 s34, v36, 2
	v_readlane_b32 s35, v36, 3
	v_readlane_b32 s36, v36, 4
	v_readlane_b32 s37, v36, 5
	v_readlane_b32 s38, v36, 6
	v_readlane_b32 s39, v36, 7
	v_readlane_b32 s40, v38, 0
	v_readlane_b32 s41, v38, 1
	v_readlane_b32 s42, v38, 2
	v_readlane_b32 s43, v38, 3
	v_readlane_b32 s44, v38, 4
	v_readlane_b32 s45, v38, 5
	v_readlane_b32 s46, v38, 6
	v_readlane_b32 s47, v38, 7
	s_waitcnt lgkmcnt(0)
	s_barrier
	s_lshl_b32 s3, s19, 10
	v_add_u32_e32 v11, s3, v10
	ds_read_b128 v[16:19], v11
	ds_read_b128 v[20:23], v11 offset:8192
	s_waitcnt lgkmcnt(0)
	s_add_u32 s3, s19, 1
	s_and_b32 s3, s3, 7
	s_lshl_b32 s57, s3, 10
	s_add_u32 s48, s57, s22
	s_add_u32 s49, s48, 0x2000
	s_add_u32 s50, s48, 0x4000
	s_add_u32 s51, s48, 0x6000
	s_add_u32 s52, s48, 0x8000
	s_add_u32 s53, s48, 0xa000
	s_add_u32 s54, s48, 0xc000
	s_add_u32 s55, s48, 0xe000
	s_lshl_b32 s56, s3, 15
	s_add_u32 s56, s56, s23
	buffer_load_dwordx4 v[120:123], v1, s[4:7], s48 offen nt
	buffer_load_dwordx4 v[124:127], v1, s[4:7], s49 offen nt
	buffer_load_dwordx4 v[128:131], v1, s[4:7], s50 offen nt
	buffer_load_dwordx4 v[132:135], v1, s[4:7], s51 offen nt
	buffer_load_dwordx4 v[136:139], v1, s[4:7], s52 offen nt
	buffer_load_dwordx4 v[140:143], v1, s[4:7], s53 offen nt
	buffer_load_dwordx4 v[144:147], v1, s[4:7], s54 offen nt
	buffer_load_dwordx4 v[148:151], v1, s[4:7], s55 offen nt
	buffer_load_dwordx4 v[168:171], v1, s[8:11], s56 offen
	buffer_load_dwordx4 v[172:175], v1, s[8:11], s56 offen offset:1024
	buffer_load_dwordx4 v[176:179], v1, s[8:11], s56 offen offset:2048
	buffer_load_dwordx4 v[180:183], v1, s[8:11], s56 offen offset:3072
	s_waitcnt vmcnt(12)
	v_mul_f32_e32 v24, s32, v16
	v_mul_f32_e32 v25, s32, v17
	v_mul_f32_e32 v26, s32, v18
	v_mul_f32_e32 v27, s32, v19
	v_mul_f32_e32 v28, s40, v20
	v_mul_f32_e32 v29, s40, v21
	v_mul_f32_e32 v30, s40, v22
	v_mul_f32_e32 v31, s40, v23
	v_cmp_lt_i32_e64 s[60:61], 0, v88
	v_cmp_lt_i32_e64 s[62:63], 0, v89
	v_cmp_lt_i32_e64 s[64:65], 0, v90
	v_cmp_lt_i32_e64 s[66:67], 0, v91
	v_max_f32_e32 v24, v24, v28
	v_max_f32_e32 v25, v25, v29
	v_max_f32_e32 v26, v26, v30
	v_max_f32_e32 v27, v27, v31
	v_cndmask_b32_e64 v24, 0, v24, s[60:61]
	v_cndmask_b32_e64 v25, 0, v25, s[62:63]
	v_cndmask_b32_e64 v26, 0, v26, s[64:65]
	v_cndmask_b32_e64 v27, 0, v27, s[66:67]
	v_cvt_pkrtz_f16_f32 v32, v24, v25
	v_cvt_pkrtz_f16_f32 v33, v26, v27
	v_mul_f32_e32 v24, s33, v16
	v_mul_f32_e32 v25, s33, v17
	v_mul_f32_e32 v26, s33, v18
	v_mul_f32_e32 v27, s33, v19
	v_mul_f32_e32 v28, s41, v20
	v_mul_f32_e32 v29, s41, v21
	v_mul_f32_e32 v30, s41, v22
	v_mul_f32_e32 v31, s41, v23
	v_cmp_lt_i32_e64 s[60:61], 0, v92
	v_cmp_lt_i32_e64 s[62:63], 0, v93
	v_cmp_lt_i32_e64 s[64:65], 0, v94
	v_cmp_lt_i32_e64 s[66:67], 0, v95
	v_max_f32_e32 v24, v24, v28
	v_max_f32_e32 v25, v25, v29
	v_max_f32_e32 v26, v26, v30
	v_max_f32_e32 v27, v27, v31
	v_cndmask_b32_e64 v24, 0, v24, s[60:61]
	v_cndmask_b32_e64 v25, 0, v25, s[62:63]
	v_cndmask_b32_e64 v26, 0, v26, s[64:65]
	v_cndmask_b32_e64 v27, 0, v27, s[66:67]
	v_cvt_pkrtz_f16_f32 v34, v24, v25
	v_cvt_pkrtz_f16_f32 v35, v26, v27
	ds_write2_b64 v3, v[32:33], v[34:35] offset0:0 offset1:66
	v_mul_f32_e32 v24, s34, v16
	v_mul_f32_e32 v25, s34, v17
	v_mul_f32_e32 v26, s34, v18
	v_mul_f32_e32 v27, s34, v19
	v_mul_f32_e32 v28, s42, v20
	v_mul_f32_e32 v29, s42, v21
	v_mul_f32_e32 v30, s42, v22
	v_mul_f32_e32 v31, s42, v23
	v_cmp_lt_i32_e64 s[60:61], 0, v96
	v_cmp_lt_i32_e64 s[62:63], 0, v97
	v_cmp_lt_i32_e64 s[64:65], 0, v98
	v_cmp_lt_i32_e64 s[66:67], 0, v99
	v_max_f32_e32 v24, v24, v28
	v_max_f32_e32 v25, v25, v29
	v_max_f32_e32 v26, v26, v30
	v_max_f32_e32 v27, v27, v31
	v_cndmask_b32_e64 v24, 0, v24, s[60:61]
	v_cndmask_b32_e64 v25, 0, v25, s[62:63]
	v_cndmask_b32_e64 v26, 0, v26, s[64:65]
	v_cndmask_b32_e64 v27, 0, v27, s[66:67]
	v_cvt_pkrtz_f16_f32 v32, v24, v25
	v_cvt_pkrtz_f16_f32 v33, v26, v27
	v_mul_f32_e32 v24, s35, v16
	v_mul_f32_e32 v25, s35, v17
	v_mul_f32_e32 v26, s35, v18
	v_mul_f32_e32 v27, s35, v19
	v_mul_f32_e32 v28, s43, v20
	v_mul_f32_e32 v29, s43, v21
	v_mul_f32_e32 v30, s43, v22
	v_mul_f32_e32 v31, s43, v23
	v_cmp_lt_i32_e64 s[60:61], 0, v100
	v_cmp_lt_i32_e64 s[62:63], 0, v101
	v_cmp_lt_i32_e64 s[64:65], 0, v102
	v_cmp_lt_i32_e64 s[66:67], 0, v103
	v_max_f32_e32 v24, v24, v28
	v_max_f32_e32 v25, v25, v29
	v_max_f32_e32 v26, v26, v30
	v_max_f32_e32 v27, v27, v31
	v_cndmask_b32_e64 v24, 0, v24, s[60:61]
	v_cndmask_b32_e64 v25, 0, v25, s[62:63]
	v_cndmask_b32_e64 v26, 0, v26, s[64:65]
	v_cndmask_b32_e64 v27, 0, v27, s[66:67]
	v_cvt_pkrtz_f16_f32 v34, v24, v25
	v_cvt_pkrtz_f16_f32 v35, v26, v27
	ds_write2_b64 v3, v[32:33], v[34:35] offset0:132 offset1:198
	v_mul_f32_e32 v24, s36, v16
	v_mul_f32_e32 v25, s36, v17
	v_mul_f32_e32 v26, s36, v18
	v_mul_f32_e32 v27, s36, v19
	v_mul_f32_e32 v28, s44, v20
	v_mul_f32_e32 v29, s44, v21
	v_mul_f32_e32 v30, s44, v22
	v_mul_f32_e32 v31, s44, v23
	v_cmp_lt_i32_e64 s[60:61], 0, v104
	v_cmp_lt_i32_e64 s[62:63], 0, v105
	v_cmp_lt_i32_e64 s[64:65], 0, v106
	v_cmp_lt_i32_e64 s[66:67], 0, v107
	v_max_f32_e32 v24, v24, v28
	v_max_f32_e32 v25, v25, v29
	v_max_f32_e32 v26, v26, v30
	v_max_f32_e32 v27, v27, v31
	v_cndmask_b32_e64 v24, 0, v24, s[60:61]
	v_cndmask_b32_e64 v25, 0, v25, s[62:63]
	v_cndmask_b32_e64 v26, 0, v26, s[64:65]
	v_cndmask_b32_e64 v27, 0, v27, s[66:67]
	v_cvt_pkrtz_f16_f32 v32, v24, v25
	v_cvt_pkrtz_f16_f32 v33, v26, v27
	v_mul_f32_e32 v24, s37, v16
	v_mul_f32_e32 v25, s37, v17
	v_mul_f32_e32 v26, s37, v18
	v_mul_f32_e32 v27, s37, v19
	v_mul_f32_e32 v28, s45, v20
	v_mul_f32_e32 v29, s45, v21
	v_mul_f32_e32 v30, s45, v22
	v_mul_f32_e32 v31, s45, v23
	v_cmp_lt_i32_e64 s[60:61], 0, v108
	v_cmp_lt_i32_e64 s[62:63], 0, v109
	v_cmp_lt_i32_e64 s[64:65], 0, v110
	v_cmp_lt_i32_e64 s[66:67], 0, v111
	v_max_f32_e32 v24, v24, v28
	v_max_f32_e32 v25, v25, v29
	v_max_f32_e32 v26, v26, v30
	v_max_f32_e32 v27, v27, v31
	v_cndmask_b32_e64 v24, 0, v24, s[60:61]
	v_cndmask_b32_e64 v25, 0, v25, s[62:63]
	v_cndmask_b32_e64 v26, 0, v26, s[64:65]
	v_cndmask_b32_e64 v27, 0, v27, s[66:67]
	v_cvt_pkrtz_f16_f32 v34, v24, v25
	v_cvt_pkrtz_f16_f32 v35, v26, v27
	ds_write2_b64 v4, v[32:33], v[34:35] offset0:0 offset1:66
	v_mul_f32_e32 v24, s38, v16
	v_mul_f32_e32 v25, s38, v17
	v_mul_f32_e32 v26, s38, v18
	v_mul_f32_e32 v27, s38, v19
	v_mul_f32_e32 v28, s46, v20
	v_mul_f32_e32 v29, s46, v21
	v_mul_f32_e32 v30, s46, v22
	v_mul_f32_e32 v31, s46, v23
	v_cmp_lt_i32_e64 s[60:61], 0, v112
	v_cmp_lt_i32_e64 s[62:63], 0, v113
	v_cmp_lt_i32_e64 s[64:65], 0, v114
	v_cmp_lt_i32_e64 s[66:67], 0, v115
	v_max_f32_e32 v24, v24, v28
	v_max_f32_e32 v25, v25, v29
	v_max_f32_e32 v26, v26, v30
	v_max_f32_e32 v27, v27, v31
	v_cndmask_b32_e64 v24, 0, v24, s[60:61]
	v_cndmask_b32_e64 v25, 0, v25, s[62:63]
	v_cndmask_b32_e64 v26, 0, v26, s[64:65]
	v_cndmask_b32_e64 v27, 0, v27, s[66:67]
	v_cvt_pkrtz_f16_f32 v32, v24, v25
	v_cvt_pkrtz_f16_f32 v33, v26, v27
	v_mul_f32_e32 v24, s39, v16
	v_mul_f32_e32 v25, s39, v17
	v_mul_f32_e32 v26, s39, v18
	v_mul_f32_e32 v27, s39, v19
	v_mul_f32_e32 v28, s47, v20
	v_mul_f32_e32 v29, s47, v21
	v_mul_f32_e32 v30, s47, v22
	v_mul_f32_e32 v31, s47, v23
	v_cmp_lt_i32_e64 s[60:61], 0, v116
	v_cmp_lt_i32_e64 s[62:63], 0, v117
	v_cmp_lt_i32_e64 s[64:65], 0, v118
	v_cmp_lt_i32_e64 s[66:67], 0, v119
	v_max_f32_e32 v24, v24, v28
	v_max_f32_e32 v25, v25, v29
	v_max_f32_e32 v26, v26, v30
	v_max_f32_e32 v27, v27, v31
	v_cndmask_b32_e64 v24, 0, v24, s[60:61]
	v_cndmask_b32_e64 v25, 0, v25, s[62:63]
	v_cndmask_b32_e64 v26, 0, v26, s[64:65]
	v_cndmask_b32_e64 v27, 0, v27, s[66:67]
	v_cvt_pkrtz_f16_f32 v34, v24, v25
	v_cvt_pkrtz_f16_f32 v35, v26, v27
	ds_write2_b64 v4, v[32:33], v[34:35] offset0:132 offset1:198
	ds_write_b128 v9, v[152:155] offset:0
	ds_write_b128 v9, v[156:159] offset:1024
	ds_write_b128 v9, v[160:163] offset:2048
	ds_write_b128 v9, v[164:167] offset:3072
	s_add_u32 s3, s19, 1
	s_and_b32 s3, s3, 7
	s_lshl_b32 s3, s3, 10
	v_add_u32_e32 v11, s3, v10
	ds_read_b128 v[16:19], v11
	ds_read_b128 v[20:23], v11 offset:8192
	s_waitcnt lgkmcnt(0)
	s_barrier
	ds_read_b128 v[184:187], v7 offset:0
	ds_read_b128 v[200:203], v8 offset:0
	ds_read_b128 v[204:207], v8 offset:1024
	ds_read_b128 v[188:191], v7 offset:32
	ds_read_b128 v[208:211], v8 offset:2048
	ds_read_b128 v[212:215], v8 offset:3072
	ds_read_b128 v[192:195], v7 offset:64
	ds_read_b128 v[216:219], v8 offset:4096
	ds_read_b128 v[220:223], v8 offset:5120
	ds_read_b128 v[196:199], v7 offset:96
	ds_read_b128 v[224:227], v8 offset:6144
	ds_read_b128 v[228:231], v8 offset:7168
	s_add_u32 s3, s19, 2
	s_and_b32 s3, s3, 7
	s_lshl_b32 s57, s3, 10
	s_add_u32 s48, s57, s22
	s_add_u32 s49, s48, 0x2000
	s_add_u32 s50, s48, 0x4000
	s_add_u32 s51, s48, 0x6000
	s_add_u32 s52, s48, 0x8000
	s_add_u32 s53, s48, 0xa000
	s_add_u32 s54, s48, 0xc000
	s_add_u32 s55, s48, 0xe000
	s_lshl_b32 s56, s3, 15
	s_add_u32 s56, s56, s23
	buffer_load_dwordx4 v[88:91], v1, s[4:7], s48 offen nt
	buffer_load_dwordx4 v[92:95], v1, s[4:7], s49 offen nt
	buffer_load_dwordx4 v[96:99], v1, s[4:7], s50 offen nt
	buffer_load_dwordx4 v[100:103], v1, s[4:7], s51 offen nt
	buffer_load_dwordx4 v[104:107], v1, s[4:7], s52 offen nt
	buffer_load_dwordx4 v[108:111], v1, s[4:7], s53 offen nt
	buffer_load_dwordx4 v[112:115], v1, s[4:7], s54 offen nt
	buffer_load_dwordx4 v[116:119], v1, s[4:7], s55 offen nt
	buffer_load_dwordx4 v[152:155], v1, s[8:11], s56 offen
	buffer_load_dwordx4 v[156:159], v1, s[8:11], s56 offen offset:1024
	buffer_load_dwordx4 v[160:163], v1, s[8:11], s56 offen offset:2048
	buffer_load_dwordx4 v[164:167], v1, s[8:11], s56 offen offset:3072
	s_waitcnt vmcnt(12)
	v_mul_f32_e32 v24, s32, v16
	v_mul_f32_e32 v25, s32, v17
	v_mul_f32_e32 v26, s32, v18
	v_mul_f32_e32 v27, s32, v19
	v_mul_f32_e32 v28, s40, v20
	v_mul_f32_e32 v29, s40, v21
	v_mul_f32_e32 v30, s40, v22
	v_mul_f32_e32 v31, s40, v23
	v_cmp_lt_i32_e64 s[60:61], 0, v120
	v_cmp_lt_i32_e64 s[62:63], 0, v121
	v_cmp_lt_i32_e64 s[64:65], 0, v122
	v_cmp_lt_i32_e64 s[66:67], 0, v123
	v_max_f32_e32 v24, v24, v28
	v_max_f32_e32 v25, v25, v29
	v_max_f32_e32 v26, v26, v30
	v_max_f32_e32 v27, v27, v31
	v_cndmask_b32_e64 v24, 0, v24, s[60:61]
	v_cndmask_b32_e64 v25, 0, v25, s[62:63]
	v_cndmask_b32_e64 v26, 0, v26, s[64:65]
	v_cndmask_b32_e64 v27, 0, v27, s[66:67]
	v_cvt_pkrtz_f16_f32 v32, v24, v25
	v_cvt_pkrtz_f16_f32 v33, v26, v27
	s_waitcnt lgkmcnt(0)
	v_mul_f32_e32 v24, s33, v16
	v_mul_f32_e32 v25, s33, v17
	v_mul_f32_e32 v26, s33, v18
	v_mul_f32_e32 v27, s33, v19
	v_mul_f32_e32 v28, s41, v20
	v_mul_f32_e32 v29, s41, v21
	v_mul_f32_e32 v30, s41, v22
	v_mul_f32_e32 v31, s41, v23
	v_mfma_f32_32x32x16_f16 v[40:55], v[184:187], v[200:203], v[40:55]
	v_cmp_lt_i32_e64 s[60:61], 0, v124
	v_cmp_lt_i32_e64 s[62:63], 0, v125
	v_cmp_lt_i32_e64 s[64:65], 0, v126
	v_cmp_lt_i32_e64 s[66:67], 0, v127
	v_max_f32_e32 v24, v24, v28
	v_max_f32_e32 v25, v25, v29
	v_max_f32_e32 v26, v26, v30
	v_max_f32_e32 v27, v27, v31
	v_cndmask_b32_e64 v24, 0, v24, s[60:61]
	v_cndmask_b32_e64 v25, 0, v25, s[62:63]
	v_cndmask_b32_e64 v26, 0, v26, s[64:65]
	v_cndmask_b32_e64 v27, 0, v27, s[66:67]
	v_mfma_f32_32x32x16_f16 v[56:71], v[184:187], v[204:207], v[56:71]
	v_cvt_pkrtz_f16_f32 v34, v24, v25
	v_cvt_pkrtz_f16_f32 v35, v26, v27
	ds_write2_b64 v5, v[32:33], v[34:35] offset0:0 offset1:66
	v_mul_f32_e32 v24, s34, v16
	v_mul_f32_e32 v25, s34, v17
	v_mul_f32_e32 v26, s34, v18
	v_mul_f32_e32 v27, s34, v19
	v_mul_f32_e32 v28, s42, v20
	v_mul_f32_e32 v29, s42, v21
	v_mul_f32_e32 v30, s42, v22
	v_mul_f32_e32 v31, s42, v23
	v_mfma_f32_32x32x16_f16 v[72:87], v[184:187], v[12:15], v[72:87]
	v_cmp_lt_i32_e64 s[60:61], 0, v128
	v_cmp_lt_i32_e64 s[62:63], 0, v129
	v_cmp_lt_i32_e64 s[64:65], 0, v130
	v_cmp_lt_i32_e64 s[66:67], 0, v131
	v_max_f32_e32 v24, v24, v28
	v_max_f32_e32 v25, v25, v29
	v_max_f32_e32 v26, v26, v30
	v_max_f32_e32 v27, v27, v31
	v_cndmask_b32_e64 v24, 0, v24, s[60:61]
	v_cndmask_b32_e64 v25, 0, v25, s[62:63]
	v_cndmask_b32_e64 v26, 0, v26, s[64:65]
	v_cndmask_b32_e64 v27, 0, v27, s[66:67]
	v_mfma_f32_32x32x16_f16 v[40:55], v[188:191], v[208:211], v[40:55]
	v_cvt_pkrtz_f16_f32 v32, v24, v25
	v_cvt_pkrtz_f16_f32 v33, v26, v27
	v_mul_f32_e32 v24, s35, v16
	v_mul_f32_e32 v25, s35, v17
	v_mul_f32_e32 v26, s35, v18
	v_mul_f32_e32 v27, s35, v19
	v_mul_f32_e32 v28, s43, v20
	v_mul_f32_e32 v29, s43, v21
	v_mul_f32_e32 v30, s43, v22
	v_mul_f32_e32 v31, s43, v23
	v_mfma_f32_32x32x16_f16 v[56:71], v[188:191], v[212:215], v[56:71]
	v_cmp_lt_i32_e64 s[60:61], 0, v132
	v_cmp_lt_i32_e64 s[62:63], 0, v133
	v_cmp_lt_i32_e64 s[64:65], 0, v134
	v_cmp_lt_i32_e64 s[66:67], 0, v135
	v_max_f32_e32 v24, v24, v28
	v_max_f32_e32 v25, v25, v29
	v_max_f32_e32 v26, v26, v30
	v_max_f32_e32 v27, v27, v31
	v_cndmask_b32_e64 v24, 0, v24, s[60:61]
	v_cndmask_b32_e64 v25, 0, v25, s[62:63]
	v_cndmask_b32_e64 v26, 0, v26, s[64:65]
	v_cndmask_b32_e64 v27, 0, v27, s[66:67]
	v_mfma_f32_32x32x16_f16 v[72:87], v[188:191], v[12:15], v[72:87]
	v_cvt_pkrtz_f16_f32 v34, v24, v25
	v_cvt_pkrtz_f16_f32 v35, v26, v27
	ds_write2_b64 v5, v[32:33], v[34:35] offset0:132 offset1:198
	v_mul_f32_e32 v24, s36, v16
	v_mul_f32_e32 v25, s36, v17
	v_mul_f32_e32 v26, s36, v18
	v_mul_f32_e32 v27, s36, v19
	v_mul_f32_e32 v28, s44, v20
	v_mul_f32_e32 v29, s44, v21
	v_mul_f32_e32 v30, s44, v22
	v_mul_f32_e32 v31, s44, v23
	v_mfma_f32_32x32x16_f16 v[40:55], v[192:195], v[216:219], v[40:55]
	v_cmp_lt_i32_e64 s[60:61], 0, v136
	v_cmp_lt_i32_e64 s[62:63], 0, v137
	v_cmp_lt_i32_e64 s[64:65], 0, v138
	v_cmp_lt_i32_e64 s[66:67], 0, v139
	v_max_f32_e32 v24, v24, v28
	v_max_f32_e32 v25, v25, v29
	v_max_f32_e32 v26, v26, v30
	v_max_f32_e32 v27, v27, v31
	v_cndmask_b32_e64 v24, 0, v24, s[60:61]
	v_cndmask_b32_e64 v25, 0, v25, s[62:63]
	v_cndmask_b32_e64 v26, 0, v26, s[64:65]
	v_cndmask_b32_e64 v27, 0, v27, s[66:67]
	v_mfma_f32_32x32x16_f16 v[56:71], v[192:195], v[220:223], v[56:71]
	v_cvt_pkrtz_f16_f32 v32, v24, v25
	v_cvt_pkrtz_f16_f32 v33, v26, v27
	v_mul_f32_e32 v24, s37, v16
	v_mul_f32_e32 v25, s37, v17
	v_mul_f32_e32 v26, s37, v18
	v_mul_f32_e32 v27, s37, v19
	v_mul_f32_e32 v28, s45, v20
	v_mul_f32_e32 v29, s45, v21
	v_mul_f32_e32 v30, s45, v22
	v_mul_f32_e32 v31, s45, v23
	v_mfma_f32_32x32x16_f16 v[72:87], v[192:195], v[12:15], v[72:87]
	v_cmp_lt_i32_e64 s[60:61], 0, v140
	v_cmp_lt_i32_e64 s[62:63], 0, v141
	v_cmp_lt_i32_e64 s[64:65], 0, v142
	v_cmp_lt_i32_e64 s[66:67], 0, v143
	v_max_f32_e32 v24, v24, v28
	v_max_f32_e32 v25, v25, v29
	v_max_f32_e32 v26, v26, v30
	v_max_f32_e32 v27, v27, v31
	v_cndmask_b32_e64 v24, 0, v24, s[60:61]
	v_cndmask_b32_e64 v25, 0, v25, s[62:63]
	v_cndmask_b32_e64 v26, 0, v26, s[64:65]
	v_cndmask_b32_e64 v27, 0, v27, s[66:67]
	v_mfma_f32_32x32x16_f16 v[40:55], v[196:199], v[224:227], v[40:55]
	v_cvt_pkrtz_f16_f32 v34, v24, v25
	v_cvt_pkrtz_f16_f32 v35, v26, v27
	ds_write2_b64 v6, v[32:33], v[34:35] offset0:0 offset1:66
	v_mul_f32_e32 v24, s38, v16
	v_mul_f32_e32 v25, s38, v17
	v_mul_f32_e32 v26, s38, v18
	v_mul_f32_e32 v27, s38, v19
	v_mul_f32_e32 v28, s46, v20
	v_mul_f32_e32 v29, s46, v21
	v_mul_f32_e32 v30, s46, v22
	v_mul_f32_e32 v31, s46, v23
	v_mfma_f32_32x32x16_f16 v[56:71], v[196:199], v[228:231], v[56:71]
	v_cmp_lt_i32_e64 s[60:61], 0, v144
	v_cmp_lt_i32_e64 s[62:63], 0, v145
	v_cmp_lt_i32_e64 s[64:65], 0, v146
	v_cmp_lt_i32_e64 s[66:67], 0, v147
	v_max_f32_e32 v24, v24, v28
	v_max_f32_e32 v25, v25, v29
	v_max_f32_e32 v26, v26, v30
	v_max_f32_e32 v27, v27, v31
	v_cndmask_b32_e64 v24, 0, v24, s[60:61]
	v_cndmask_b32_e64 v25, 0, v25, s[62:63]
	v_cndmask_b32_e64 v26, 0, v26, s[64:65]
	v_cndmask_b32_e64 v27, 0, v27, s[66:67]
	v_cvt_pkrtz_f16_f32 v32, v24, v25
	v_cvt_pkrtz_f16_f32 v33, v26, v27
	v_mul_f32_e32 v24, s39, v16
	v_mul_f32_e32 v25, s39, v17
	v_mul_f32_e32 v26, s39, v18
	v_mul_f32_e32 v27, s39, v19
	v_mul_f32_e32 v28, s47, v20
	v_mul_f32_e32 v29, s47, v21
	v_mul_f32_e32 v30, s47, v22
	v_mul_f32_e32 v31, s47, v23
	v_mfma_f32_32x32x16_f16 v[72:87], v[196:199], v[12:15], v[72:87]
	v_cmp_lt_i32_e64 s[60:61], 0, v148
	v_cmp_lt_i32_e64 s[62:63], 0, v149
	v_cmp_lt_i32_e64 s[64:65], 0, v150
	v_cmp_lt_i32_e64 s[66:67], 0, v151
	v_max_f32_e32 v24, v24, v28
	v_max_f32_e32 v25, v25, v29
	v_max_f32_e32 v26, v26, v30
	v_max_f32_e32 v27, v27, v31
	v_cndmask_b32_e64 v24, 0, v24, s[60:61]
	v_cndmask_b32_e64 v25, 0, v25, s[62:63]
	v_cndmask_b32_e64 v26, 0, v26, s[64:65]
	v_cndmask_b32_e64 v27, 0, v27, s[66:67]
	v_cvt_pkrtz_f16_f32 v34, v24, v25
	v_cvt_pkrtz_f16_f32 v35, v26, v27
	ds_write2_b64 v6, v[32:33], v[34:35] offset0:132 offset1:198
	ds_write_b128 v9, v[168:171] offset:32768
	ds_write_b128 v9, v[172:175] offset:33792
	ds_write_b128 v9, v[176:179] offset:34816
	ds_write_b128 v9, v[180:183] offset:35840
	s_add_u32 s3, s19, 2
	s_and_b32 s3, s3, 7
	s_lshl_b32 s3, s3, 10
	v_add_u32_e32 v11, s3, v10
	ds_read_b128 v[16:19], v11
	ds_read_b128 v[20:23], v11 offset:8192
	s_waitcnt lgkmcnt(0)
	s_barrier
	ds_read_b128 v[184:187], v7 offset:33792
	ds_read_b128 v[200:203], v8 offset:32768
	ds_read_b128 v[204:207], v8 offset:33792
	ds_read_b128 v[188:191], v7 offset:33824
	ds_read_b128 v[208:211], v8 offset:34816
	ds_read_b128 v[212:215], v8 offset:35840
	ds_read_b128 v[192:195], v7 offset:33856
	ds_read_b128 v[216:219], v8 offset:36864
	ds_read_b128 v[220:223], v8 offset:37888
	ds_read_b128 v[196:199], v7 offset:33888
	ds_read_b128 v[224:227], v8 offset:38912
	ds_read_b128 v[228:231], v8 offset:39936
	s_add_u32 s3, s19, 3
	s_and_b32 s3, s3, 7
	s_lshl_b32 s57, s3, 10
	s_add_u32 s48, s57, s22
	s_add_u32 s49, s48, 0x2000
	s_add_u32 s50, s48, 0x4000
	s_add_u32 s51, s48, 0x6000
	s_add_u32 s52, s48, 0x8000
	s_add_u32 s53, s48, 0xa000
	s_add_u32 s54, s48, 0xc000
	s_add_u32 s55, s48, 0xe000
	s_lshl_b32 s56, s3, 15
	s_add_u32 s56, s56, s23
	buffer_load_dwordx4 v[120:123], v1, s[4:7], s48 offen nt
	buffer_load_dwordx4 v[124:127], v1, s[4:7], s49 offen nt
	buffer_load_dwordx4 v[128:131], v1, s[4:7], s50 offen nt
	buffer_load_dwordx4 v[132:135], v1, s[4:7], s51 offen nt
	buffer_load_dwordx4 v[136:139], v1, s[4:7], s52 offen nt
	buffer_load_dwordx4 v[140:143], v1, s[4:7], s53 offen nt
	buffer_load_dwordx4 v[144:147], v1, s[4:7], s54 offen nt
	buffer_load_dwordx4 v[148:151], v1, s[4:7], s55 offen nt
	buffer_load_dwordx4 v[168:171], v1, s[8:11], s56 offen
	buffer_load_dwordx4 v[172:175], v1, s[8:11], s56 offen offset:1024
	buffer_load_dwordx4 v[176:179], v1, s[8:11], s56 offen offset:2048
	buffer_load_dwordx4 v[180:183], v1, s[8:11], s56 offen offset:3072
	s_waitcnt vmcnt(12)
	v_mul_f32_e32 v24, s32, v16
	v_mul_f32_e32 v25, s32, v17
	v_mul_f32_e32 v26, s32, v18
	v_mul_f32_e32 v27, s32, v19
	v_mul_f32_e32 v28, s40, v20
	v_mul_f32_e32 v29, s40, v21
	v_mul_f32_e32 v30, s40, v22
	v_mul_f32_e32 v31, s40, v23
	v_cmp_lt_i32_e64 s[60:61], 0, v88
	v_cmp_lt_i32_e64 s[62:63], 0, v89
	v_cmp_lt_i32_e64 s[64:65], 0, v90
	v_cmp_lt_i32_e64 s[66:67], 0, v91
	v_max_f32_e32 v24, v24, v28
	v_max_f32_e32 v25, v25, v29
	v_max_f32_e32 v26, v26, v30
	v_max_f32_e32 v27, v27, v31
	v_cndmask_b32_e64 v24, 0, v24, s[60:61]
	v_cndmask_b32_e64 v25, 0, v25, s[62:63]
	v_cndmask_b32_e64 v26, 0, v26, s[64:65]
	v_cndmask_b32_e64 v27, 0, v27, s[66:67]
	v_cvt_pkrtz_f16_f32 v32, v24, v25
	v_cvt_pkrtz_f16_f32 v33, v26, v27
	s_waitcnt lgkmcnt(0)
	v_mul_f32_e32 v24, s33, v16
	v_mul_f32_e32 v25, s33, v17
	v_mul_f32_e32 v26, s33, v18
	v_mul_f32_e32 v27, s33, v19
	v_mul_f32_e32 v28, s41, v20
	v_mul_f32_e32 v29, s41, v21
	v_mul_f32_e32 v30, s41, v22
	v_mul_f32_e32 v31, s41, v23
	v_mfma_f32_32x32x16_f16 v[40:55], v[184:187], v[200:203], v[40:55]
	v_cmp_lt_i32_e64 s[60:61], 0, v92
	v_cmp_lt_i32_e64 s[62:63], 0, v93
	v_cmp_lt_i32_e64 s[64:65], 0, v94
	v_cmp_lt_i32_e64 s[66:67], 0, v95
	v_max_f32_e32 v24, v24, v28
	v_max_f32_e32 v25, v25, v29
	v_max_f32_e32 v26, v26, v30
	v_max_f32_e32 v27, v27, v31
	v_cndmask_b32_e64 v24, 0, v24, s[60:61]
	v_cndmask_b32_e64 v25, 0, v25, s[62:63]
	v_cndmask_b32_e64 v26, 0, v26, s[64:65]
	v_cndmask_b32_e64 v27, 0, v27, s[66:67]
	v_mfma_f32_32x32x16_f16 v[56:71], v[184:187], v[204:207], v[56:71]
	v_cvt_pkrtz_f16_f32 v34, v24, v25
	v_cvt_pkrtz_f16_f32 v35, v26, v27
	ds_write2_b64 v3, v[32:33], v[34:35] offset0:0 offset1:66
	v_mul_f32_e32 v24, s34, v16
	v_mul_f32_e32 v25, s34, v17
	v_mul_f32_e32 v26, s34, v18
	v_mul_f32_e32 v27, s34, v19
	v_mul_f32_e32 v28, s42, v20
	v_mul_f32_e32 v29, s42, v21
	v_mul_f32_e32 v30, s42, v22
	v_mul_f32_e32 v31, s42, v23
	v_mfma_f32_32x32x16_f16 v[72:87], v[184:187], v[12:15], v[72:87]
	v_cmp_lt_i32_e64 s[60:61], 0, v96
	v_cmp_lt_i32_e64 s[62:63], 0, v97
	v_cmp_lt_i32_e64 s[64:65], 0, v98
	v_cmp_lt_i32_e64 s[66:67], 0, v99
	v_max_f32_e32 v24, v24, v28
	v_max_f32_e32 v25, v25, v29
	v_max_f32_e32 v26, v26, v30
	v_max_f32_e32 v27, v27, v31
	v_cndmask_b32_e64 v24, 0, v24, s[60:61]
	v_cndmask_b32_e64 v25, 0, v25, s[62:63]
	v_cndmask_b32_e64 v26, 0, v26, s[64:65]
	v_cndmask_b32_e64 v27, 0, v27, s[66:67]
	v_mfma_f32_32x32x16_f16 v[40:55], v[188:191], v[208:211], v[40:55]
	v_cvt_pkrtz_f16_f32 v32, v24, v25
	v_cvt_pkrtz_f16_f32 v33, v26, v27
	v_mul_f32_e32 v24, s35, v16
	v_mul_f32_e32 v25, s35, v17
	v_mul_f32_e32 v26, s35, v18
	v_mul_f32_e32 v27, s35, v19
	v_mul_f32_e32 v28, s43, v20
	v_mul_f32_e32 v29, s43, v21
	v_mul_f32_e32 v30, s43, v22
	v_mul_f32_e32 v31, s43, v23
	v_mfma_f32_32x32x16_f16 v[56:71], v[188:191], v[212:215], v[56:71]
	v_cmp_lt_i32_e64 s[60:61], 0, v100
	v_cmp_lt_i32_e64 s[62:63], 0, v101
	v_cmp_lt_i32_e64 s[64:65], 0, v102
	v_cmp_lt_i32_e64 s[66:67], 0, v103
	v_max_f32_e32 v24, v24, v28
	v_max_f32_e32 v25, v25, v29
	v_max_f32_e32 v26, v26, v30
	v_max_f32_e32 v27, v27, v31
	v_cndmask_b32_e64 v24, 0, v24, s[60:61]
	v_cndmask_b32_e64 v25, 0, v25, s[62:63]
	v_cndmask_b32_e64 v26, 0, v26, s[64:65]
	v_cndmask_b32_e64 v27, 0, v27, s[66:67]
	v_mfma_f32_32x32x16_f16 v[72:87], v[188:191], v[12:15], v[72:87]
	v_cvt_pkrtz_f16_f32 v34, v24, v25
	v_cvt_pkrtz_f16_f32 v35, v26, v27
	ds_write2_b64 v3, v[32:33], v[34:35] offset0:132 offset1:198
	v_mul_f32_e32 v24, s36, v16
	v_mul_f32_e32 v25, s36, v17
	v_mul_f32_e32 v26, s36, v18
	v_mul_f32_e32 v27, s36, v19
	v_mul_f32_e32 v28, s44, v20
	v_mul_f32_e32 v29, s44, v21
	v_mul_f32_e32 v30, s44, v22
	v_mul_f32_e32 v31, s44, v23
	v_mfma_f32_32x32x16_f16 v[40:55], v[192:195], v[216:219], v[40:55]
	v_cmp_lt_i32_e64 s[60:61], 0, v104
	v_cmp_lt_i32_e64 s[62:63], 0, v105
	v_cmp_lt_i32_e64 s[64:65], 0, v106
	v_cmp_lt_i32_e64 s[66:67], 0, v107
	v_max_f32_e32 v24, v24, v28
	v_max_f32_e32 v25, v25, v29
	v_max_f32_e32 v26, v26, v30
	v_max_f32_e32 v27, v27, v31
	v_cndmask_b32_e64 v24, 0, v24, s[60:61]
	v_cndmask_b32_e64 v25, 0, v25, s[62:63]
	v_cndmask_b32_e64 v26, 0, v26, s[64:65]
	v_cndmask_b32_e64 v27, 0, v27, s[66:67]
	v_mfma_f32_32x32x16_f16 v[56:71], v[192:195], v[220:223], v[56:71]
	v_cvt_pkrtz_f16_f32 v32, v24, v25
	v_cvt_pkrtz_f16_f32 v33, v26, v27
	v_mul_f32_e32 v24, s37, v16
	v_mul_f32_e32 v25, s37, v17
	v_mul_f32_e32 v26, s37, v18
	v_mul_f32_e32 v27, s37, v19
	v_mul_f32_e32 v28, s45, v20
	v_mul_f32_e32 v29, s45, v21
	v_mul_f32_e32 v30, s45, v22
	v_mul_f32_e32 v31, s45, v23
	v_mfma_f32_32x32x16_f16 v[72:87], v[192:195], v[12:15], v[72:87]
	v_cmp_lt_i32_e64 s[60:61], 0, v108
	v_cmp_lt_i32_e64 s[62:63], 0, v109
	v_cmp_lt_i32_e64 s[64:65], 0, v110
	v_cmp_lt_i32_e64 s[66:67], 0, v111
	v_max_f32_e32 v24, v24, v28
	v_max_f32_e32 v25, v25, v29
	v_max_f32_e32 v26, v26, v30
	v_max_f32_e32 v27, v27, v31
	v_cndmask_b32_e64 v24, 0, v24, s[60:61]
	v_cndmask_b32_e64 v25, 0, v25, s[62:63]
	v_cndmask_b32_e64 v26, 0, v26, s[64:65]
	v_cndmask_b32_e64 v27, 0, v27, s[66:67]
	v_mfma_f32_32x32x16_f16 v[40:55], v[196:199], v[224:227], v[40:55]
	v_cvt_pkrtz_f16_f32 v34, v24, v25
	v_cvt_pkrtz_f16_f32 v35, v26, v27
	ds_write2_b64 v4, v[32:33], v[34:35] offset0:0 offset1:66
	v_mul_f32_e32 v24, s38, v16
	v_mul_f32_e32 v25, s38, v17
	v_mul_f32_e32 v26, s38, v18
	v_mul_f32_e32 v27, s38, v19
	v_mul_f32_e32 v28, s46, v20
	v_mul_f32_e32 v29, s46, v21
	v_mul_f32_e32 v30, s46, v22
	v_mul_f32_e32 v31, s46, v23
	v_mfma_f32_32x32x16_f16 v[56:71], v[196:199], v[228:231], v[56:71]
	v_cmp_lt_i32_e64 s[60:61], 0, v112
	v_cmp_lt_i32_e64 s[62:63], 0, v113
	v_cmp_lt_i32_e64 s[64:65], 0, v114
	v_cmp_lt_i32_e64 s[66:67], 0, v115
	v_max_f32_e32 v24, v24, v28
	v_max_f32_e32 v25, v25, v29
	v_max_f32_e32 v26, v26, v30
	v_max_f32_e32 v27, v27, v31
	v_cndmask_b32_e64 v24, 0, v24, s[60:61]
	v_cndmask_b32_e64 v25, 0, v25, s[62:63]
	v_cndmask_b32_e64 v26, 0, v26, s[64:65]
	v_cndmask_b32_e64 v27, 0, v27, s[66:67]
	v_cvt_pkrtz_f16_f32 v32, v24, v25
	v_cvt_pkrtz_f16_f32 v33, v26, v27
	v_mul_f32_e32 v24, s39, v16
	v_mul_f32_e32 v25, s39, v17
	v_mul_f32_e32 v26, s39, v18
	v_mul_f32_e32 v27, s39, v19
	v_mul_f32_e32 v28, s47, v20
	v_mul_f32_e32 v29, s47, v21
	v_mul_f32_e32 v30, s47, v22
	v_mul_f32_e32 v31, s47, v23
	v_mfma_f32_32x32x16_f16 v[72:87], v[196:199], v[12:15], v[72:87]
	v_cmp_lt_i32_e64 s[60:61], 0, v116
	v_cmp_lt_i32_e64 s[62:63], 0, v117
	v_cmp_lt_i32_e64 s[64:65], 0, v118
	v_cmp_lt_i32_e64 s[66:67], 0, v119
	v_max_f32_e32 v24, v24, v28
	v_max_f32_e32 v25, v25, v29
	v_max_f32_e32 v26, v26, v30
	v_max_f32_e32 v27, v27, v31
	v_cndmask_b32_e64 v24, 0, v24, s[60:61]
	v_cndmask_b32_e64 v25, 0, v25, s[62:63]
	v_cndmask_b32_e64 v26, 0, v26, s[64:65]
	v_cndmask_b32_e64 v27, 0, v27, s[66:67]
	v_cvt_pkrtz_f16_f32 v34, v24, v25
	v_cvt_pkrtz_f16_f32 v35, v26, v27
	ds_write2_b64 v4, v[32:33], v[34:35] offset0:132 offset1:198
	ds_write_b128 v9, v[152:155] offset:0
	ds_write_b128 v9, v[156:159] offset:1024
	ds_write_b128 v9, v[160:163] offset:2048
	ds_write_b128 v9, v[164:167] offset:3072
	s_add_u32 s3, s19, 3
	s_and_b32 s3, s3, 7
	s_lshl_b32 s3, s3, 10
	v_add_u32_e32 v11, s3, v10
	ds_read_b128 v[16:19], v11
	ds_read_b128 v[20:23], v11 offset:8192
	s_waitcnt lgkmcnt(0)
	s_barrier
	ds_read_b128 v[184:187], v7 offset:0
	ds_read_b128 v[200:203], v8 offset:0
	ds_read_b128 v[204:207], v8 offset:1024
	ds_read_b128 v[188:191], v7 offset:32
	ds_read_b128 v[208:211], v8 offset:2048
	ds_read_b128 v[212:215], v8 offset:3072
	ds_read_b128 v[192:195], v7 offset:64
	ds_read_b128 v[216:219], v8 offset:4096
	ds_read_b128 v[220:223], v8 offset:5120
	ds_read_b128 v[196:199], v7 offset:96
	ds_read_b128 v[224:227], v8 offset:6144
	ds_read_b128 v[228:231], v8 offset:7168
	s_add_u32 s3, s19, 4
	s_and_b32 s3, s3, 7
	s_lshl_b32 s57, s3, 10
	s_add_u32 s48, s57, s22
	s_add_u32 s49, s48, 0x2000
	s_add_u32 s50, s48, 0x4000
	s_add_u32 s51, s48, 0x6000
	s_add_u32 s52, s48, 0x8000
	s_add_u32 s53, s48, 0xa000
	s_add_u32 s54, s48, 0xc000
	s_add_u32 s55, s48, 0xe000
	s_lshl_b32 s56, s3, 15
	s_add_u32 s56, s56, s23
	buffer_load_dwordx4 v[88:91], v1, s[4:7], s48 offen nt
	buffer_load_dwordx4 v[92:95], v1, s[4:7], s49 offen nt
	buffer_load_dwordx4 v[96:99], v1, s[4:7], s50 offen nt
	buffer_load_dwordx4 v[100:103], v1, s[4:7], s51 offen nt
	buffer_load_dwordx4 v[104:107], v1, s[4:7], s52 offen nt
	buffer_load_dwordx4 v[108:111], v1, s[4:7], s53 offen nt
	buffer_load_dwordx4 v[112:115], v1, s[4:7], s54 offen nt
	buffer_load_dwordx4 v[116:119], v1, s[4:7], s55 offen nt
	buffer_load_dwordx4 v[152:155], v1, s[8:11], s56 offen
	buffer_load_dwordx4 v[156:159], v1, s[8:11], s56 offen offset:1024
	buffer_load_dwordx4 v[160:163], v1, s[8:11], s56 offen offset:2048
	buffer_load_dwordx4 v[164:167], v1, s[8:11], s56 offen offset:3072
	s_waitcnt vmcnt(12)
	v_mul_f32_e32 v24, s32, v16
	v_mul_f32_e32 v25, s32, v17
	v_mul_f32_e32 v26, s32, v18
	v_mul_f32_e32 v27, s32, v19
	v_mul_f32_e32 v28, s40, v20
	v_mul_f32_e32 v29, s40, v21
	v_mul_f32_e32 v30, s40, v22
	v_mul_f32_e32 v31, s40, v23
	v_cmp_lt_i32_e64 s[60:61], 0, v120
	v_cmp_lt_i32_e64 s[62:63], 0, v121
	v_cmp_lt_i32_e64 s[64:65], 0, v122
	v_cmp_lt_i32_e64 s[66:67], 0, v123
	v_max_f32_e32 v24, v24, v28
	v_max_f32_e32 v25, v25, v29
	v_max_f32_e32 v26, v26, v30
	v_max_f32_e32 v27, v27, v31
	v_cndmask_b32_e64 v24, 0, v24, s[60:61]
	v_cndmask_b32_e64 v25, 0, v25, s[62:63]
	v_cndmask_b32_e64 v26, 0, v26, s[64:65]
	v_cndmask_b32_e64 v27, 0, v27, s[66:67]
	v_cvt_pkrtz_f16_f32 v32, v24, v25
	v_cvt_pkrtz_f16_f32 v33, v26, v27
	s_waitcnt lgkmcnt(0)
	v_mul_f32_e32 v24, s33, v16
	v_mul_f32_e32 v25, s33, v17
	v_mul_f32_e32 v26, s33, v18
	v_mul_f32_e32 v27, s33, v19
	v_mul_f32_e32 v28, s41, v20
	v_mul_f32_e32 v29, s41, v21
	v_mul_f32_e32 v30, s41, v22
	v_mul_f32_e32 v31, s41, v23
	v_mfma_f32_32x32x16_f16 v[40:55], v[184:187], v[200:203], v[40:55]
	v_cmp_lt_i32_e64 s[60:61], 0, v124
	v_cmp_lt_i32_e64 s[62:63], 0, v125
	v_cmp_lt_i32_e64 s[64:65], 0, v126
	v_cmp_lt_i32_e64 s[66:67], 0, v127
	v_max_f32_e32 v24, v24, v28
	v_max_f32_e32 v25, v25, v29
	v_max_f32_e32 v26, v26, v30
	v_max_f32_e32 v27, v27, v31
	v_cndmask_b32_e64 v24, 0, v24, s[60:61]
	v_cndmask_b32_e64 v25, 0, v25, s[62:63]
	v_cndmask_b32_e64 v26, 0, v26, s[64:65]
	v_cndmask_b32_e64 v27, 0, v27, s[66:67]
	v_mfma_f32_32x32x16_f16 v[56:71], v[184:187], v[204:207], v[56:71]
	v_cvt_pkrtz_f16_f32 v34, v24, v25
	v_cvt_pkrtz_f16_f32 v35, v26, v27
	ds_write2_b64 v5, v[32:33], v[34:35] offset0:0 offset1:66
	v_mul_f32_e32 v24, s34, v16
	v_mul_f32_e32 v25, s34, v17
	v_mul_f32_e32 v26, s34, v18
	v_mul_f32_e32 v27, s34, v19
	v_mul_f32_e32 v28, s42, v20
	v_mul_f32_e32 v29, s42, v21
	v_mul_f32_e32 v30, s42, v22
	v_mul_f32_e32 v31, s42, v23
	v_mfma_f32_32x32x16_f16 v[72:87], v[184:187], v[12:15], v[72:87]
	v_cmp_lt_i32_e64 s[60:61], 0, v128
	v_cmp_lt_i32_e64 s[62:63], 0, v129
	v_cmp_lt_i32_e64 s[64:65], 0, v130
	v_cmp_lt_i32_e64 s[66:67], 0, v131
	v_max_f32_e32 v24, v24, v28
	v_max_f32_e32 v25, v25, v29
	v_max_f32_e32 v26, v26, v30
	v_max_f32_e32 v27, v27, v31
	v_cndmask_b32_e64 v24, 0, v24, s[60:61]
	v_cndmask_b32_e64 v25, 0, v25, s[62:63]
	v_cndmask_b32_e64 v26, 0, v26, s[64:65]
	v_cndmask_b32_e64 v27, 0, v27, s[66:67]
	v_mfma_f32_32x32x16_f16 v[40:55], v[188:191], v[208:211], v[40:55]
	v_cvt_pkrtz_f16_f32 v32, v24, v25
	v_cvt_pkrtz_f16_f32 v33, v26, v27
	v_mul_f32_e32 v24, s35, v16
	v_mul_f32_e32 v25, s35, v17
	v_mul_f32_e32 v26, s35, v18
	v_mul_f32_e32 v27, s35, v19
	v_mul_f32_e32 v28, s43, v20
	v_mul_f32_e32 v29, s43, v21
	v_mul_f32_e32 v30, s43, v22
	v_mul_f32_e32 v31, s43, v23
	v_mfma_f32_32x32x16_f16 v[56:71], v[188:191], v[212:215], v[56:71]
	v_cmp_lt_i32_e64 s[60:61], 0, v132
	v_cmp_lt_i32_e64 s[62:63], 0, v133
	v_cmp_lt_i32_e64 s[64:65], 0, v134
	v_cmp_lt_i32_e64 s[66:67], 0, v135
	v_max_f32_e32 v24, v24, v28
	v_max_f32_e32 v25, v25, v29
	v_max_f32_e32 v26, v26, v30
	v_max_f32_e32 v27, v27, v31
	v_cndmask_b32_e64 v24, 0, v24, s[60:61]
	v_cndmask_b32_e64 v25, 0, v25, s[62:63]
	v_cndmask_b32_e64 v26, 0, v26, s[64:65]
	v_cndmask_b32_e64 v27, 0, v27, s[66:67]
	v_mfma_f32_32x32x16_f16 v[72:87], v[188:191], v[12:15], v[72:87]
	v_cvt_pkrtz_f16_f32 v34, v24, v25
	v_cvt_pkrtz_f16_f32 v35, v26, v27
	ds_write2_b64 v5, v[32:33], v[34:35] offset0:132 offset1:198
	v_mul_f32_e32 v24, s36, v16
	v_mul_f32_e32 v25, s36, v17
	v_mul_f32_e32 v26, s36, v18
	v_mul_f32_e32 v27, s36, v19
	v_mul_f32_e32 v28, s44, v20
	v_mul_f32_e32 v29, s44, v21
	v_mul_f32_e32 v30, s44, v22
	v_mul_f32_e32 v31, s44, v23
	v_mfma_f32_32x32x16_f16 v[40:55], v[192:195], v[216:219], v[40:55]
	v_cmp_lt_i32_e64 s[60:61], 0, v136
	v_cmp_lt_i32_e64 s[62:63], 0, v137
	v_cmp_lt_i32_e64 s[64:65], 0, v138
	v_cmp_lt_i32_e64 s[66:67], 0, v139
	v_max_f32_e32 v24, v24, v28
	v_max_f32_e32 v25, v25, v29
	v_max_f32_e32 v26, v26, v30
	v_max_f32_e32 v27, v27, v31
	v_cndmask_b32_e64 v24, 0, v24, s[60:61]
	v_cndmask_b32_e64 v25, 0, v25, s[62:63]
	v_cndmask_b32_e64 v26, 0, v26, s[64:65]
	v_cndmask_b32_e64 v27, 0, v27, s[66:67]
	v_mfma_f32_32x32x16_f16 v[56:71], v[192:195], v[220:223], v[56:71]
	v_cvt_pkrtz_f16_f32 v32, v24, v25
	v_cvt_pkrtz_f16_f32 v33, v26, v27
	v_mul_f32_e32 v24, s37, v16
	v_mul_f32_e32 v25, s37, v17
	v_mul_f32_e32 v26, s37, v18
	v_mul_f32_e32 v27, s37, v19
	v_mul_f32_e32 v28, s45, v20
	v_mul_f32_e32 v29, s45, v21
	v_mul_f32_e32 v30, s45, v22
	v_mul_f32_e32 v31, s45, v23
	v_mfma_f32_32x32x16_f16 v[72:87], v[192:195], v[12:15], v[72:87]
	v_cmp_lt_i32_e64 s[60:61], 0, v140
	v_cmp_lt_i32_e64 s[62:63], 0, v141
	v_cmp_lt_i32_e64 s[64:65], 0, v142
	v_cmp_lt_i32_e64 s[66:67], 0, v143
	v_max_f32_e32 v24, v24, v28
	v_max_f32_e32 v25, v25, v29
	v_max_f32_e32 v26, v26, v30
	v_max_f32_e32 v27, v27, v31
	v_cndmask_b32_e64 v24, 0, v24, s[60:61]
	v_cndmask_b32_e64 v25, 0, v25, s[62:63]
	v_cndmask_b32_e64 v26, 0, v26, s[64:65]
	v_cndmask_b32_e64 v27, 0, v27, s[66:67]
	v_mfma_f32_32x32x16_f16 v[40:55], v[196:199], v[224:227], v[40:55]
	v_cvt_pkrtz_f16_f32 v34, v24, v25
	v_cvt_pkrtz_f16_f32 v35, v26, v27
	ds_write2_b64 v6, v[32:33], v[34:35] offset0:0 offset1:66
	v_mul_f32_e32 v24, s38, v16
	v_mul_f32_e32 v25, s38, v17
	v_mul_f32_e32 v26, s38, v18
	v_mul_f32_e32 v27, s38, v19
	v_mul_f32_e32 v28, s46, v20
	v_mul_f32_e32 v29, s46, v21
	v_mul_f32_e32 v30, s46, v22
	v_mul_f32_e32 v31, s46, v23
	v_mfma_f32_32x32x16_f16 v[56:71], v[196:199], v[228:231], v[56:71]
	v_cmp_lt_i32_e64 s[60:61], 0, v144
	v_cmp_lt_i32_e64 s[62:63], 0, v145
	v_cmp_lt_i32_e64 s[64:65], 0, v146
	v_cmp_lt_i32_e64 s[66:67], 0, v147
	v_max_f32_e32 v24, v24, v28
	v_max_f32_e32 v25, v25, v29
	v_max_f32_e32 v26, v26, v30
	v_max_f32_e32 v27, v27, v31
	v_cndmask_b32_e64 v24, 0, v24, s[60:61]
	v_cndmask_b32_e64 v25, 0, v25, s[62:63]
	v_cndmask_b32_e64 v26, 0, v26, s[64:65]
	v_cndmask_b32_e64 v27, 0, v27, s[66:67]
	v_cvt_pkrtz_f16_f32 v32, v24, v25
	v_cvt_pkrtz_f16_f32 v33, v26, v27
	v_mul_f32_e32 v24, s39, v16
	v_mul_f32_e32 v25, s39, v17
	v_mul_f32_e32 v26, s39, v18
	v_mul_f32_e32 v27, s39, v19
	v_mul_f32_e32 v28, s47, v20
	v_mul_f32_e32 v29, s47, v21
	v_mul_f32_e32 v30, s47, v22
	v_mul_f32_e32 v31, s47, v23
	v_mfma_f32_32x32x16_f16 v[72:87], v[196:199], v[12:15], v[72:87]
	v_cmp_lt_i32_e64 s[60:61], 0, v148
	v_cmp_lt_i32_e64 s[62:63], 0, v149
	v_cmp_lt_i32_e64 s[64:65], 0, v150
	v_cmp_lt_i32_e64 s[66:67], 0, v151
	v_max_f32_e32 v24, v24, v28
	v_max_f32_e32 v25, v25, v29
	v_max_f32_e32 v26, v26, v30
	v_max_f32_e32 v27, v27, v31
	v_cndmask_b32_e64 v24, 0, v24, s[60:61]
	v_cndmask_b32_e64 v25, 0, v25, s[62:63]
	v_cndmask_b32_e64 v26, 0, v26, s[64:65]
	v_cndmask_b32_e64 v27, 0, v27, s[66:67]
	v_cvt_pkrtz_f16_f32 v34, v24, v25
	v_cvt_pkrtz_f16_f32 v35, v26, v27
	ds_write2_b64 v6, v[32:33], v[34:35] offset0:132 offset1:198
	ds_write_b128 v9, v[168:171] offset:32768
	ds_write_b128 v9, v[172:175] offset:33792
	ds_write_b128 v9, v[176:179] offset:34816
	ds_write_b128 v9, v[180:183] offset:35840
	s_add_u32 s3, s19, 4
	s_and_b32 s3, s3, 7
	s_lshl_b32 s3, s3, 10
	v_add_u32_e32 v11, s3, v10
	ds_read_b128 v[16:19], v11
	ds_read_b128 v[20:23], v11 offset:8192
	s_waitcnt lgkmcnt(0)
	s_barrier
	ds_read_b128 v[184:187], v7 offset:33792
	ds_read_b128 v[200:203], v8 offset:32768
	ds_read_b128 v[204:207], v8 offset:33792
	ds_read_b128 v[188:191], v7 offset:33824
	ds_read_b128 v[208:211], v8 offset:34816
	ds_read_b128 v[212:215], v8 offset:35840
	ds_read_b128 v[192:195], v7 offset:33856
	ds_read_b128 v[216:219], v8 offset:36864
	ds_read_b128 v[220:223], v8 offset:37888
	ds_read_b128 v[196:199], v7 offset:33888
	ds_read_b128 v[224:227], v8 offset:38912
	ds_read_b128 v[228:231], v8 offset:39936
	s_add_u32 s3, s19, 5
	s_and_b32 s3, s3, 7
	s_lshl_b32 s57, s3, 10
	s_add_u32 s48, s57, s22
	s_add_u32 s49, s48, 0x2000
	s_add_u32 s50, s48, 0x4000
	s_add_u32 s51, s48, 0x6000
	s_add_u32 s52, s48, 0x8000
	s_add_u32 s53, s48, 0xa000
	s_add_u32 s54, s48, 0xc000
	s_add_u32 s55, s48, 0xe000
	s_lshl_b32 s56, s3, 15
	s_add_u32 s56, s56, s23
	buffer_load_dwordx4 v[120:123], v1, s[4:7], s48 offen nt
	buffer_load_dwordx4 v[124:127], v1, s[4:7], s49 offen nt
	buffer_load_dwordx4 v[128:131], v1, s[4:7], s50 offen nt
	buffer_load_dwordx4 v[132:135], v1, s[4:7], s51 offen nt
	buffer_load_dwordx4 v[136:139], v1, s[4:7], s52 offen nt
	buffer_load_dwordx4 v[140:143], v1, s[4:7], s53 offen nt
	buffer_load_dwordx4 v[144:147], v1, s[4:7], s54 offen nt
	buffer_load_dwordx4 v[148:151], v1, s[4:7], s55 offen nt
	buffer_load_dwordx4 v[168:171], v1, s[8:11], s56 offen
	buffer_load_dwordx4 v[172:175], v1, s[8:11], s56 offen offset:1024
	buffer_load_dwordx4 v[176:179], v1, s[8:11], s56 offen offset:2048
	buffer_load_dwordx4 v[180:183], v1, s[8:11], s56 offen offset:3072
	s_waitcnt vmcnt(12)
	v_mul_f32_e32 v24, s32, v16
	v_mul_f32_e32 v25, s32, v17
	v_mul_f32_e32 v26, s32, v18
	v_mul_f32_e32 v27, s32, v19
	v_mul_f32_e32 v28, s40, v20
	v_mul_f32_e32 v29, s40, v21
	v_mul_f32_e32 v30, s40, v22
	v_mul_f32_e32 v31, s40, v23
	v_cmp_lt_i32_e64 s[60:61], 0, v88
	v_cmp_lt_i32_e64 s[62:63], 0, v89
	v_cmp_lt_i32_e64 s[64:65], 0, v90
	v_cmp_lt_i32_e64 s[66:67], 0, v91
	v_max_f32_e32 v24, v24, v28
	v_max_f32_e32 v25, v25, v29
	v_max_f32_e32 v26, v26, v30
	v_max_f32_e32 v27, v27, v31
	v_cndmask_b32_e64 v24, 0, v24, s[60:61]
	v_cndmask_b32_e64 v25, 0, v25, s[62:63]
	v_cndmask_b32_e64 v26, 0, v26, s[64:65]
	v_cndmask_b32_e64 v27, 0, v27, s[66:67]
	v_cvt_pkrtz_f16_f32 v32, v24, v25
	v_cvt_pkrtz_f16_f32 v33, v26, v27
	s_waitcnt lgkmcnt(0)
	v_mul_f32_e32 v24, s33, v16
	v_mul_f32_e32 v25, s33, v17
	v_mul_f32_e32 v26, s33, v18
	v_mul_f32_e32 v27, s33, v19
	v_mul_f32_e32 v28, s41, v20
	v_mul_f32_e32 v29, s41, v21
	v_mul_f32_e32 v30, s41, v22
	v_mul_f32_e32 v31, s41, v23
	v_mfma_f32_32x32x16_f16 v[40:55], v[184:187], v[200:203], v[40:55]
	v_cmp_lt_i32_e64 s[60:61], 0, v92
	v_cmp_lt_i32_e64 s[62:63], 0, v93
	v_cmp_lt_i32_e64 s[64:65], 0, v94
	v_cmp_lt_i32_e64 s[66:67], 0, v95
	v_max_f32_e32 v24, v24, v28
	v_max_f32_e32 v25, v25, v29
	v_max_f32_e32 v26, v26, v30
	v_max_f32_e32 v27, v27, v31
	v_cndmask_b32_e64 v24, 0, v24, s[60:61]
	v_cndmask_b32_e64 v25, 0, v25, s[62:63]
	v_cndmask_b32_e64 v26, 0, v26, s[64:65]
	v_cndmask_b32_e64 v27, 0, v27, s[66:67]
	v_mfma_f32_32x32x16_f16 v[56:71], v[184:187], v[204:207], v[56:71]
	v_cvt_pkrtz_f16_f32 v34, v24, v25
	v_cvt_pkrtz_f16_f32 v35, v26, v27
	ds_write2_b64 v3, v[32:33], v[34:35] offset0:0 offset1:66
	v_mul_f32_e32 v24, s34, v16
	v_mul_f32_e32 v25, s34, v17
	v_mul_f32_e32 v26, s34, v18
	v_mul_f32_e32 v27, s34, v19
	v_mul_f32_e32 v28, s42, v20
	v_mul_f32_e32 v29, s42, v21
	v_mul_f32_e32 v30, s42, v22
	v_mul_f32_e32 v31, s42, v23
	v_mfma_f32_32x32x16_f16 v[72:87], v[184:187], v[12:15], v[72:87]
	v_cmp_lt_i32_e64 s[60:61], 0, v96
	v_cmp_lt_i32_e64 s[62:63], 0, v97
	v_cmp_lt_i32_e64 s[64:65], 0, v98
	v_cmp_lt_i32_e64 s[66:67], 0, v99
	v_max_f32_e32 v24, v24, v28
	v_max_f32_e32 v25, v25, v29
	v_max_f32_e32 v26, v26, v30
	v_max_f32_e32 v27, v27, v31
	v_cndmask_b32_e64 v24, 0, v24, s[60:61]
	v_cndmask_b32_e64 v25, 0, v25, s[62:63]
	v_cndmask_b32_e64 v26, 0, v26, s[64:65]
	v_cndmask_b32_e64 v27, 0, v27, s[66:67]
	v_mfma_f32_32x32x16_f16 v[40:55], v[188:191], v[208:211], v[40:55]
	v_cvt_pkrtz_f16_f32 v32, v24, v25
	v_cvt_pkrtz_f16_f32 v33, v26, v27
	v_mul_f32_e32 v24, s35, v16
	v_mul_f32_e32 v25, s35, v17
	v_mul_f32_e32 v26, s35, v18
	v_mul_f32_e32 v27, s35, v19
	v_mul_f32_e32 v28, s43, v20
	v_mul_f32_e32 v29, s43, v21
	v_mul_f32_e32 v30, s43, v22
	v_mul_f32_e32 v31, s43, v23
	v_mfma_f32_32x32x16_f16 v[56:71], v[188:191], v[212:215], v[56:71]
	v_cmp_lt_i32_e64 s[60:61], 0, v100
	v_cmp_lt_i32_e64 s[62:63], 0, v101
	v_cmp_lt_i32_e64 s[64:65], 0, v102
	v_cmp_lt_i32_e64 s[66:67], 0, v103
	v_max_f32_e32 v24, v24, v28
	v_max_f32_e32 v25, v25, v29
	v_max_f32_e32 v26, v26, v30
	v_max_f32_e32 v27, v27, v31
	v_cndmask_b32_e64 v24, 0, v24, s[60:61]
	v_cndmask_b32_e64 v25, 0, v25, s[62:63]
	v_cndmask_b32_e64 v26, 0, v26, s[64:65]
	v_cndmask_b32_e64 v27, 0, v27, s[66:67]
	v_mfma_f32_32x32x16_f16 v[72:87], v[188:191], v[12:15], v[72:87]
	v_cvt_pkrtz_f16_f32 v34, v24, v25
	v_cvt_pkrtz_f16_f32 v35, v26, v27
	ds_write2_b64 v3, v[32:33], v[34:35] offset0:132 offset1:198
	v_mul_f32_e32 v24, s36, v16
	v_mul_f32_e32 v25, s36, v17
	v_mul_f32_e32 v26, s36, v18
	v_mul_f32_e32 v27, s36, v19
	v_mul_f32_e32 v28, s44, v20
	v_mul_f32_e32 v29, s44, v21
	v_mul_f32_e32 v30, s44, v22
	v_mul_f32_e32 v31, s44, v23
	v_mfma_f32_32x32x16_f16 v[40:55], v[192:195], v[216:219], v[40:55]
	v_cmp_lt_i32_e64 s[60:61], 0, v104
	v_cmp_lt_i32_e64 s[62:63], 0, v105
	v_cmp_lt_i32_e64 s[64:65], 0, v106
	v_cmp_lt_i32_e64 s[66:67], 0, v107
	v_max_f32_e32 v24, v24, v28
	v_max_f32_e32 v25, v25, v29
	v_max_f32_e32 v26, v26, v30
	v_max_f32_e32 v27, v27, v31
	v_cndmask_b32_e64 v24, 0, v24, s[60:61]
	v_cndmask_b32_e64 v25, 0, v25, s[62:63]
	v_cndmask_b32_e64 v26, 0, v26, s[64:65]
	v_cndmask_b32_e64 v27, 0, v27, s[66:67]
	v_mfma_f32_32x32x16_f16 v[56:71], v[192:195], v[220:223], v[56:71]
	v_cvt_pkrtz_f16_f32 v32, v24, v25
	v_cvt_pkrtz_f16_f32 v33, v26, v27
	v_mul_f32_e32 v24, s37, v16
	v_mul_f32_e32 v25, s37, v17
	v_mul_f32_e32 v26, s37, v18
	v_mul_f32_e32 v27, s37, v19
	v_mul_f32_e32 v28, s45, v20
	v_mul_f32_e32 v29, s45, v21
	v_mul_f32_e32 v30, s45, v22
	v_mul_f32_e32 v31, s45, v23
	v_mfma_f32_32x32x16_f16 v[72:87], v[192:195], v[12:15], v[72:87]
	v_cmp_lt_i32_e64 s[60:61], 0, v108
	v_cmp_lt_i32_e64 s[62:63], 0, v109
	v_cmp_lt_i32_e64 s[64:65], 0, v110
	v_cmp_lt_i32_e64 s[66:67], 0, v111
	v_max_f32_e32 v24, v24, v28
	v_max_f32_e32 v25, v25, v29
	v_max_f32_e32 v26, v26, v30
	v_max_f32_e32 v27, v27, v31
	v_cndmask_b32_e64 v24, 0, v24, s[60:61]
	v_cndmask_b32_e64 v25, 0, v25, s[62:63]
	v_cndmask_b32_e64 v26, 0, v26, s[64:65]
	v_cndmask_b32_e64 v27, 0, v27, s[66:67]
	v_mfma_f32_32x32x16_f16 v[40:55], v[196:199], v[224:227], v[40:55]
	v_cvt_pkrtz_f16_f32 v34, v24, v25
	v_cvt_pkrtz_f16_f32 v35, v26, v27
	ds_write2_b64 v4, v[32:33], v[34:35] offset0:0 offset1:66
	v_mul_f32_e32 v24, s38, v16
	v_mul_f32_e32 v25, s38, v17
	v_mul_f32_e32 v26, s38, v18
	v_mul_f32_e32 v27, s38, v19
	v_mul_f32_e32 v28, s46, v20
	v_mul_f32_e32 v29, s46, v21
	v_mul_f32_e32 v30, s46, v22
	v_mul_f32_e32 v31, s46, v23
	v_mfma_f32_32x32x16_f16 v[56:71], v[196:199], v[228:231], v[56:71]
	v_cmp_lt_i32_e64 s[60:61], 0, v112
	v_cmp_lt_i32_e64 s[62:63], 0, v113
	v_cmp_lt_i32_e64 s[64:65], 0, v114
	v_cmp_lt_i32_e64 s[66:67], 0, v115
	v_max_f32_e32 v24, v24, v28
	v_max_f32_e32 v25, v25, v29
	v_max_f32_e32 v26, v26, v30
	v_max_f32_e32 v27, v27, v31
	v_cndmask_b32_e64 v24, 0, v24, s[60:61]
	v_cndmask_b32_e64 v25, 0, v25, s[62:63]
	v_cndmask_b32_e64 v26, 0, v26, s[64:65]
	v_cndmask_b32_e64 v27, 0, v27, s[66:67]
	v_cvt_pkrtz_f16_f32 v32, v24, v25
	v_cvt_pkrtz_f16_f32 v33, v26, v27
	v_mul_f32_e32 v24, s39, v16
	v_mul_f32_e32 v25, s39, v17
	v_mul_f32_e32 v26, s39, v18
	v_mul_f32_e32 v27, s39, v19
	v_mul_f32_e32 v28, s47, v20
	v_mul_f32_e32 v29, s47, v21
	v_mul_f32_e32 v30, s47, v22
	v_mul_f32_e32 v31, s47, v23
	v_mfma_f32_32x32x16_f16 v[72:87], v[196:199], v[12:15], v[72:87]
	v_cmp_lt_i32_e64 s[60:61], 0, v116
	v_cmp_lt_i32_e64 s[62:63], 0, v117
	v_cmp_lt_i32_e64 s[64:65], 0, v118
	v_cmp_lt_i32_e64 s[66:67], 0, v119
	v_max_f32_e32 v24, v24, v28
	v_max_f32_e32 v25, v25, v29
	v_max_f32_e32 v26, v26, v30
	v_max_f32_e32 v27, v27, v31
	v_cndmask_b32_e64 v24, 0, v24, s[60:61]
	v_cndmask_b32_e64 v25, 0, v25, s[62:63]
	v_cndmask_b32_e64 v26, 0, v26, s[64:65]
	v_cndmask_b32_e64 v27, 0, v27, s[66:67]
	v_cvt_pkrtz_f16_f32 v34, v24, v25
	v_cvt_pkrtz_f16_f32 v35, v26, v27
	ds_write2_b64 v4, v[32:33], v[34:35] offset0:132 offset1:198
	ds_write_b128 v9, v[152:155] offset:0
	ds_write_b128 v9, v[156:159] offset:1024
	ds_write_b128 v9, v[160:163] offset:2048
	ds_write_b128 v9, v[164:167] offset:3072
	s_add_u32 s3, s19, 5
	s_and_b32 s3, s3, 7
	s_lshl_b32 s3, s3, 10
	v_add_u32_e32 v11, s3, v10
	ds_read_b128 v[16:19], v11
	ds_read_b128 v[20:23], v11 offset:8192
	s_waitcnt lgkmcnt(0)
	s_barrier
	ds_read_b128 v[184:187], v7 offset:0
	ds_read_b128 v[200:203], v8 offset:0
	ds_read_b128 v[204:207], v8 offset:1024
	ds_read_b128 v[188:191], v7 offset:32
	ds_read_b128 v[208:211], v8 offset:2048
	ds_read_b128 v[212:215], v8 offset:3072
	ds_read_b128 v[192:195], v7 offset:64
	ds_read_b128 v[216:219], v8 offset:4096
	ds_read_b128 v[220:223], v8 offset:5120
	ds_read_b128 v[196:199], v7 offset:96
	ds_read_b128 v[224:227], v8 offset:6144
	ds_read_b128 v[228:231], v8 offset:7168
	s_add_u32 s3, s19, 6
	s_and_b32 s3, s3, 7
	s_lshl_b32 s57, s3, 10
	s_add_u32 s48, s57, s22
	s_add_u32 s49, s48, 0x2000
	s_add_u32 s50, s48, 0x4000
	s_add_u32 s51, s48, 0x6000
	s_add_u32 s52, s48, 0x8000
	s_add_u32 s53, s48, 0xa000
	s_add_u32 s54, s48, 0xc000
	s_add_u32 s55, s48, 0xe000
	s_lshl_b32 s56, s3, 15
	s_add_u32 s56, s56, s23
	buffer_load_dwordx4 v[88:91], v1, s[4:7], s48 offen nt
	buffer_load_dwordx4 v[92:95], v1, s[4:7], s49 offen nt
	buffer_load_dwordx4 v[96:99], v1, s[4:7], s50 offen nt
	buffer_load_dwordx4 v[100:103], v1, s[4:7], s51 offen nt
	buffer_load_dwordx4 v[104:107], v1, s[4:7], s52 offen nt
	buffer_load_dwordx4 v[108:111], v1, s[4:7], s53 offen nt
	buffer_load_dwordx4 v[112:115], v1, s[4:7], s54 offen nt
	buffer_load_dwordx4 v[116:119], v1, s[4:7], s55 offen nt
	buffer_load_dwordx4 v[152:155], v1, s[8:11], s56 offen
	buffer_load_dwordx4 v[156:159], v1, s[8:11], s56 offen offset:1024
	buffer_load_dwordx4 v[160:163], v1, s[8:11], s56 offen offset:2048
	buffer_load_dwordx4 v[164:167], v1, s[8:11], s56 offen offset:3072
	s_waitcnt vmcnt(12)
	v_mul_f32_e32 v24, s32, v16
	v_mul_f32_e32 v25, s32, v17
	v_mul_f32_e32 v26, s32, v18
	v_mul_f32_e32 v27, s32, v19
	v_mul_f32_e32 v28, s40, v20
	v_mul_f32_e32 v29, s40, v21
	v_mul_f32_e32 v30, s40, v22
	v_mul_f32_e32 v31, s40, v23
	v_cmp_lt_i32_e64 s[60:61], 0, v120
	v_cmp_lt_i32_e64 s[62:63], 0, v121
	v_cmp_lt_i32_e64 s[64:65], 0, v122
	v_cmp_lt_i32_e64 s[66:67], 0, v123
	v_max_f32_e32 v24, v24, v28
	v_max_f32_e32 v25, v25, v29
	v_max_f32_e32 v26, v26, v30
	v_max_f32_e32 v27, v27, v31
	v_cndmask_b32_e64 v24, 0, v24, s[60:61]
	v_cndmask_b32_e64 v25, 0, v25, s[62:63]
	v_cndmask_b32_e64 v26, 0, v26, s[64:65]
	v_cndmask_b32_e64 v27, 0, v27, s[66:67]
	v_cvt_pkrtz_f16_f32 v32, v24, v25
	v_cvt_pkrtz_f16_f32 v33, v26, v27
	s_waitcnt lgkmcnt(0)
	v_mul_f32_e32 v24, s33, v16
	v_mul_f32_e32 v25, s33, v17
	v_mul_f32_e32 v26, s33, v18
	v_mul_f32_e32 v27, s33, v19
	v_mul_f32_e32 v28, s41, v20
	v_mul_f32_e32 v29, s41, v21
	v_mul_f32_e32 v30, s41, v22
	v_mul_f32_e32 v31, s41, v23
	v_mfma_f32_32x32x16_f16 v[40:55], v[184:187], v[200:203], v[40:55]
	v_cmp_lt_i32_e64 s[60:61], 0, v124
	v_cmp_lt_i32_e64 s[62:63], 0, v125
	v_cmp_lt_i32_e64 s[64:65], 0, v126
	v_cmp_lt_i32_e64 s[66:67], 0, v127
	v_max_f32_e32 v24, v24, v28
	v_max_f32_e32 v25, v25, v29
	v_max_f32_e32 v26, v26, v30
	v_max_f32_e32 v27, v27, v31
	v_cndmask_b32_e64 v24, 0, v24, s[60:61]
	v_cndmask_b32_e64 v25, 0, v25, s[62:63]
	v_cndmask_b32_e64 v26, 0, v26, s[64:65]
	v_cndmask_b32_e64 v27, 0, v27, s[66:67]
	v_mfma_f32_32x32x16_f16 v[56:71], v[184:187], v[204:207], v[56:71]
	v_cvt_pkrtz_f16_f32 v34, v24, v25
	v_cvt_pkrtz_f16_f32 v35, v26, v27
	ds_write2_b64 v5, v[32:33], v[34:35] offset0:0 offset1:66
	v_mul_f32_e32 v24, s34, v16
	v_mul_f32_e32 v25, s34, v17
	v_mul_f32_e32 v26, s34, v18
	v_mul_f32_e32 v27, s34, v19
	v_mul_f32_e32 v28, s42, v20
	v_mul_f32_e32 v29, s42, v21
	v_mul_f32_e32 v30, s42, v22
	v_mul_f32_e32 v31, s42, v23
	v_mfma_f32_32x32x16_f16 v[72:87], v[184:187], v[12:15], v[72:87]
	v_cmp_lt_i32_e64 s[60:61], 0, v128
	v_cmp_lt_i32_e64 s[62:63], 0, v129
	v_cmp_lt_i32_e64 s[64:65], 0, v130
	v_cmp_lt_i32_e64 s[66:67], 0, v131
	v_max_f32_e32 v24, v24, v28
	v_max_f32_e32 v25, v25, v29
	v_max_f32_e32 v26, v26, v30
	v_max_f32_e32 v27, v27, v31
	v_cndmask_b32_e64 v24, 0, v24, s[60:61]
	v_cndmask_b32_e64 v25, 0, v25, s[62:63]
	v_cndmask_b32_e64 v26, 0, v26, s[64:65]
	v_cndmask_b32_e64 v27, 0, v27, s[66:67]
	v_mfma_f32_32x32x16_f16 v[40:55], v[188:191], v[208:211], v[40:55]
	v_cvt_pkrtz_f16_f32 v32, v24, v25
	v_cvt_pkrtz_f16_f32 v33, v26, v27
	v_mul_f32_e32 v24, s35, v16
	v_mul_f32_e32 v25, s35, v17
	v_mul_f32_e32 v26, s35, v18
	v_mul_f32_e32 v27, s35, v19
	v_mul_f32_e32 v28, s43, v20
	v_mul_f32_e32 v29, s43, v21
	v_mul_f32_e32 v30, s43, v22
	v_mul_f32_e32 v31, s43, v23
	v_mfma_f32_32x32x16_f16 v[56:71], v[188:191], v[212:215], v[56:71]
	v_cmp_lt_i32_e64 s[60:61], 0, v132
	v_cmp_lt_i32_e64 s[62:63], 0, v133
	v_cmp_lt_i32_e64 s[64:65], 0, v134
	v_cmp_lt_i32_e64 s[66:67], 0, v135
	v_max_f32_e32 v24, v24, v28
	v_max_f32_e32 v25, v25, v29
	v_max_f32_e32 v26, v26, v30
	v_max_f32_e32 v27, v27, v31
	v_cndmask_b32_e64 v24, 0, v24, s[60:61]
	v_cndmask_b32_e64 v25, 0, v25, s[62:63]
	v_cndmask_b32_e64 v26, 0, v26, s[64:65]
	v_cndmask_b32_e64 v27, 0, v27, s[66:67]
	v_mfma_f32_32x32x16_f16 v[72:87], v[188:191], v[12:15], v[72:87]
	v_cvt_pkrtz_f16_f32 v34, v24, v25
	v_cvt_pkrtz_f16_f32 v35, v26, v27
	ds_write2_b64 v5, v[32:33], v[34:35] offset0:132 offset1:198
	v_mul_f32_e32 v24, s36, v16
	v_mul_f32_e32 v25, s36, v17
	v_mul_f32_e32 v26, s36, v18
	v_mul_f32_e32 v27, s36, v19
	v_mul_f32_e32 v28, s44, v20
	v_mul_f32_e32 v29, s44, v21
	v_mul_f32_e32 v30, s44, v22
	v_mul_f32_e32 v31, s44, v23
	v_mfma_f32_32x32x16_f16 v[40:55], v[192:195], v[216:219], v[40:55]
	v_cmp_lt_i32_e64 s[60:61], 0, v136
	v_cmp_lt_i32_e64 s[62:63], 0, v137
	v_cmp_lt_i32_e64 s[64:65], 0, v138
	v_cmp_lt_i32_e64 s[66:67], 0, v139
	v_max_f32_e32 v24, v24, v28
	v_max_f32_e32 v25, v25, v29
	v_max_f32_e32 v26, v26, v30
	v_max_f32_e32 v27, v27, v31
	v_cndmask_b32_e64 v24, 0, v24, s[60:61]
	v_cndmask_b32_e64 v25, 0, v25, s[62:63]
	v_cndmask_b32_e64 v26, 0, v26, s[64:65]
	v_cndmask_b32_e64 v27, 0, v27, s[66:67]
	v_mfma_f32_32x32x16_f16 v[56:71], v[192:195], v[220:223], v[56:71]
	v_cvt_pkrtz_f16_f32 v32, v24, v25
	v_cvt_pkrtz_f16_f32 v33, v26, v27
	v_mul_f32_e32 v24, s37, v16
	v_mul_f32_e32 v25, s37, v17
	v_mul_f32_e32 v26, s37, v18
	v_mul_f32_e32 v27, s37, v19
	v_mul_f32_e32 v28, s45, v20
	v_mul_f32_e32 v29, s45, v21
	v_mul_f32_e32 v30, s45, v22
	v_mul_f32_e32 v31, s45, v23
	v_mfma_f32_32x32x16_f16 v[72:87], v[192:195], v[12:15], v[72:87]
	v_cmp_lt_i32_e64 s[60:61], 0, v140
	v_cmp_lt_i32_e64 s[62:63], 0, v141
	v_cmp_lt_i32_e64 s[64:65], 0, v142
	v_cmp_lt_i32_e64 s[66:67], 0, v143
	v_max_f32_e32 v24, v24, v28
	v_max_f32_e32 v25, v25, v29
	v_max_f32_e32 v26, v26, v30
	v_max_f32_e32 v27, v27, v31
	v_cndmask_b32_e64 v24, 0, v24, s[60:61]
	v_cndmask_b32_e64 v25, 0, v25, s[62:63]
	v_cndmask_b32_e64 v26, 0, v26, s[64:65]
	v_cndmask_b32_e64 v27, 0, v27, s[66:67]
	v_mfma_f32_32x32x16_f16 v[40:55], v[196:199], v[224:227], v[40:55]
	v_cvt_pkrtz_f16_f32 v34, v24, v25
	v_cvt_pkrtz_f16_f32 v35, v26, v27
	ds_write2_b64 v6, v[32:33], v[34:35] offset0:0 offset1:66
	v_mul_f32_e32 v24, s38, v16
	v_mul_f32_e32 v25, s38, v17
	v_mul_f32_e32 v26, s38, v18
	v_mul_f32_e32 v27, s38, v19
	v_mul_f32_e32 v28, s46, v20
	v_mul_f32_e32 v29, s46, v21
	v_mul_f32_e32 v30, s46, v22
	v_mul_f32_e32 v31, s46, v23
	v_mfma_f32_32x32x16_f16 v[56:71], v[196:199], v[228:231], v[56:71]
	v_cmp_lt_i32_e64 s[60:61], 0, v144
	v_cmp_lt_i32_e64 s[62:63], 0, v145
	v_cmp_lt_i32_e64 s[64:65], 0, v146
	v_cmp_lt_i32_e64 s[66:67], 0, v147
	v_max_f32_e32 v24, v24, v28
	v_max_f32_e32 v25, v25, v29
	v_max_f32_e32 v26, v26, v30
	v_max_f32_e32 v27, v27, v31
	v_cndmask_b32_e64 v24, 0, v24, s[60:61]
	v_cndmask_b32_e64 v25, 0, v25, s[62:63]
	v_cndmask_b32_e64 v26, 0, v26, s[64:65]
	v_cndmask_b32_e64 v27, 0, v27, s[66:67]
	v_cvt_pkrtz_f16_f32 v32, v24, v25
	v_cvt_pkrtz_f16_f32 v33, v26, v27
	v_mul_f32_e32 v24, s39, v16
	v_mul_f32_e32 v25, s39, v17
	v_mul_f32_e32 v26, s39, v18
	v_mul_f32_e32 v27, s39, v19
	v_mul_f32_e32 v28, s47, v20
	v_mul_f32_e32 v29, s47, v21
	v_mul_f32_e32 v30, s47, v22
	v_mul_f32_e32 v31, s47, v23
	v_mfma_f32_32x32x16_f16 v[72:87], v[196:199], v[12:15], v[72:87]
	v_cmp_lt_i32_e64 s[60:61], 0, v148
	v_cmp_lt_i32_e64 s[62:63], 0, v149
	v_cmp_lt_i32_e64 s[64:65], 0, v150
	v_cmp_lt_i32_e64 s[66:67], 0, v151
	v_max_f32_e32 v24, v24, v28
	v_max_f32_e32 v25, v25, v29
	v_max_f32_e32 v26, v26, v30
	v_max_f32_e32 v27, v27, v31
	v_cndmask_b32_e64 v24, 0, v24, s[60:61]
	v_cndmask_b32_e64 v25, 0, v25, s[62:63]
	v_cndmask_b32_e64 v26, 0, v26, s[64:65]
	v_cndmask_b32_e64 v27, 0, v27, s[66:67]
	v_cvt_pkrtz_f16_f32 v34, v24, v25
	v_cvt_pkrtz_f16_f32 v35, v26, v27
	ds_write2_b64 v6, v[32:33], v[34:35] offset0:132 offset1:198
	ds_write_b128 v9, v[168:171] offset:32768
	ds_write_b128 v9, v[172:175] offset:33792
	ds_write_b128 v9, v[176:179] offset:34816
	ds_write_b128 v9, v[180:183] offset:35840
	s_add_u32 s3, s19, 6
	s_and_b32 s3, s3, 7
	s_lshl_b32 s3, s3, 10
	v_add_u32_e32 v11, s3, v10
	ds_read_b128 v[16:19], v11
	ds_read_b128 v[20:23], v11 offset:8192
	s_waitcnt lgkmcnt(0)
	s_barrier
	ds_read_b128 v[184:187], v7 offset:33792
	ds_read_b128 v[200:203], v8 offset:32768
	ds_read_b128 v[204:207], v8 offset:33792
	ds_read_b128 v[188:191], v7 offset:33824
	ds_read_b128 v[208:211], v8 offset:34816
	ds_read_b128 v[212:215], v8 offset:35840
	ds_read_b128 v[192:195], v7 offset:33856
	ds_read_b128 v[216:219], v8 offset:36864
	ds_read_b128 v[220:223], v8 offset:37888
	ds_read_b128 v[196:199], v7 offset:33888
	ds_read_b128 v[224:227], v8 offset:38912
	ds_read_b128 v[228:231], v8 offset:39936
	s_add_u32 s3, s19, 7
	s_and_b32 s3, s3, 7
	s_lshl_b32 s57, s3, 10
	s_add_u32 s48, s57, s22
	s_add_u32 s49, s48, 0x2000
	s_add_u32 s50, s48, 0x4000
	s_add_u32 s51, s48, 0x6000
	s_add_u32 s52, s48, 0x8000
	s_add_u32 s53, s48, 0xa000
	s_add_u32 s54, s48, 0xc000
	s_add_u32 s55, s48, 0xe000
	s_lshl_b32 s56, s3, 15
	s_add_u32 s56, s56, s23
	buffer_load_dwordx4 v[120:123], v1, s[4:7], s48 offen nt
	buffer_load_dwordx4 v[124:127], v1, s[4:7], s49 offen nt
	buffer_load_dwordx4 v[128:131], v1, s[4:7], s50 offen nt
	buffer_load_dwordx4 v[132:135], v1, s[4:7], s51 offen nt
	buffer_load_dwordx4 v[136:139], v1, s[4:7], s52 offen nt
	buffer_load_dwordx4 v[140:143], v1, s[4:7], s53 offen nt
	buffer_load_dwordx4 v[144:147], v1, s[4:7], s54 offen nt
	buffer_load_dwordx4 v[148:151], v1, s[4:7], s55 offen nt
	buffer_load_dwordx4 v[168:171], v1, s[8:11], s56 offen
	buffer_load_dwordx4 v[172:175], v1, s[8:11], s56 offen offset:1024
	buffer_load_dwordx4 v[176:179], v1, s[8:11], s56 offen offset:2048
	buffer_load_dwordx4 v[180:183], v1, s[8:11], s56 offen offset:3072
	s_waitcnt vmcnt(12)
	v_mul_f32_e32 v24, s32, v16
	v_mul_f32_e32 v25, s32, v17
	v_mul_f32_e32 v26, s32, v18
	v_mul_f32_e32 v27, s32, v19
	v_mul_f32_e32 v28, s40, v20
	v_mul_f32_e32 v29, s40, v21
	v_mul_f32_e32 v30, s40, v22
	v_mul_f32_e32 v31, s40, v23
	v_cmp_lt_i32_e64 s[60:61], 0, v88
	v_cmp_lt_i32_e64 s[62:63], 0, v89
	v_cmp_lt_i32_e64 s[64:65], 0, v90
	v_cmp_lt_i32_e64 s[66:67], 0, v91
	v_max_f32_e32 v24, v24, v28
	v_max_f32_e32 v25, v25, v29
	v_max_f32_e32 v26, v26, v30
	v_max_f32_e32 v27, v27, v31
	v_cndmask_b32_e64 v24, 0, v24, s[60:61]
	v_cndmask_b32_e64 v25, 0, v25, s[62:63]
	v_cndmask_b32_e64 v26, 0, v26, s[64:65]
	v_cndmask_b32_e64 v27, 0, v27, s[66:67]
	v_cvt_pkrtz_f16_f32 v32, v24, v25
	v_cvt_pkrtz_f16_f32 v33, v26, v27
	s_waitcnt lgkmcnt(0)
	v_mul_f32_e32 v24, s33, v16
	v_mul_f32_e32 v25, s33, v17
	v_mul_f32_e32 v26, s33, v18
	v_mul_f32_e32 v27, s33, v19
	v_mul_f32_e32 v28, s41, v20
	v_mul_f32_e32 v29, s41, v21
	v_mul_f32_e32 v30, s41, v22
	v_mul_f32_e32 v31, s41, v23
	v_mfma_f32_32x32x16_f16 v[40:55], v[184:187], v[200:203], v[40:55]
	v_cmp_lt_i32_e64 s[60:61], 0, v92
	v_cmp_lt_i32_e64 s[62:63], 0, v93
	v_cmp_lt_i32_e64 s[64:65], 0, v94
	v_cmp_lt_i32_e64 s[66:67], 0, v95
	v_max_f32_e32 v24, v24, v28
	v_max_f32_e32 v25, v25, v29
	v_max_f32_e32 v26, v26, v30
	v_max_f32_e32 v27, v27, v31
	v_cndmask_b32_e64 v24, 0, v24, s[60:61]
	v_cndmask_b32_e64 v25, 0, v25, s[62:63]
	v_cndmask_b32_e64 v26, 0, v26, s[64:65]
	v_cndmask_b32_e64 v27, 0, v27, s[66:67]
	v_mfma_f32_32x32x16_f16 v[56:71], v[184:187], v[204:207], v[56:71]
	v_cvt_pkrtz_f16_f32 v34, v24, v25
	v_cvt_pkrtz_f16_f32 v35, v26, v27
	ds_write2_b64 v3, v[32:33], v[34:35] offset0:0 offset1:66
	v_mul_f32_e32 v24, s34, v16
	v_mul_f32_e32 v25, s34, v17
	v_mul_f32_e32 v26, s34, v18
	v_mul_f32_e32 v27, s34, v19
	v_mul_f32_e32 v28, s42, v20
	v_mul_f32_e32 v29, s42, v21
	v_mul_f32_e32 v30, s42, v22
	v_mul_f32_e32 v31, s42, v23
	v_mfma_f32_32x32x16_f16 v[72:87], v[184:187], v[12:15], v[72:87]
	v_cmp_lt_i32_e64 s[60:61], 0, v96
	v_cmp_lt_i32_e64 s[62:63], 0, v97
	v_cmp_lt_i32_e64 s[64:65], 0, v98
	v_cmp_lt_i32_e64 s[66:67], 0, v99
	v_max_f32_e32 v24, v24, v28
	v_max_f32_e32 v25, v25, v29
	v_max_f32_e32 v26, v26, v30
	v_max_f32_e32 v27, v27, v31
	v_cndmask_b32_e64 v24, 0, v24, s[60:61]
	v_cndmask_b32_e64 v25, 0, v25, s[62:63]
	v_cndmask_b32_e64 v26, 0, v26, s[64:65]
	v_cndmask_b32_e64 v27, 0, v27, s[66:67]
	v_mfma_f32_32x32x16_f16 v[40:55], v[188:191], v[208:211], v[40:55]
	v_cvt_pkrtz_f16_f32 v32, v24, v25
	v_cvt_pkrtz_f16_f32 v33, v26, v27
	v_mul_f32_e32 v24, s35, v16
	v_mul_f32_e32 v25, s35, v17
	v_mul_f32_e32 v26, s35, v18
	v_mul_f32_e32 v27, s35, v19
	v_mul_f32_e32 v28, s43, v20
	v_mul_f32_e32 v29, s43, v21
	v_mul_f32_e32 v30, s43, v22
	v_mul_f32_e32 v31, s43, v23
	v_mfma_f32_32x32x16_f16 v[56:71], v[188:191], v[212:215], v[56:71]
	v_cmp_lt_i32_e64 s[60:61], 0, v100
	v_cmp_lt_i32_e64 s[62:63], 0, v101
	v_cmp_lt_i32_e64 s[64:65], 0, v102
	v_cmp_lt_i32_e64 s[66:67], 0, v103
	v_max_f32_e32 v24, v24, v28
	v_max_f32_e32 v25, v25, v29
	v_max_f32_e32 v26, v26, v30
	v_max_f32_e32 v27, v27, v31
	v_cndmask_b32_e64 v24, 0, v24, s[60:61]
	v_cndmask_b32_e64 v25, 0, v25, s[62:63]
	v_cndmask_b32_e64 v26, 0, v26, s[64:65]
	v_cndmask_b32_e64 v27, 0, v27, s[66:67]
	v_mfma_f32_32x32x16_f16 v[72:87], v[188:191], v[12:15], v[72:87]
	v_cvt_pkrtz_f16_f32 v34, v24, v25
	v_cvt_pkrtz_f16_f32 v35, v26, v27
	ds_write2_b64 v3, v[32:33], v[34:35] offset0:132 offset1:198
	v_mul_f32_e32 v24, s36, v16
	v_mul_f32_e32 v25, s36, v17
	v_mul_f32_e32 v26, s36, v18
	v_mul_f32_e32 v27, s36, v19
	v_mul_f32_e32 v28, s44, v20
	v_mul_f32_e32 v29, s44, v21
	v_mul_f32_e32 v30, s44, v22
	v_mul_f32_e32 v31, s44, v23
	v_mfma_f32_32x32x16_f16 v[40:55], v[192:195], v[216:219], v[40:55]
	v_cmp_lt_i32_e64 s[60:61], 0, v104
	v_cmp_lt_i32_e64 s[62:63], 0, v105
	v_cmp_lt_i32_e64 s[64:65], 0, v106
	v_cmp_lt_i32_e64 s[66:67], 0, v107
	v_max_f32_e32 v24, v24, v28
	v_max_f32_e32 v25, v25, v29
	v_max_f32_e32 v26, v26, v30
	v_max_f32_e32 v27, v27, v31
	v_cndmask_b32_e64 v24, 0, v24, s[60:61]
	v_cndmask_b32_e64 v25, 0, v25, s[62:63]
	v_cndmask_b32_e64 v26, 0, v26, s[64:65]
	v_cndmask_b32_e64 v27, 0, v27, s[66:67]
	v_mfma_f32_32x32x16_f16 v[56:71], v[192:195], v[220:223], v[56:71]
	v_cvt_pkrtz_f16_f32 v32, v24, v25
	v_cvt_pkrtz_f16_f32 v33, v26, v27
	v_mul_f32_e32 v24, s37, v16
	v_mul_f32_e32 v25, s37, v17
	v_mul_f32_e32 v26, s37, v18
	v_mul_f32_e32 v27, s37, v19
	v_mul_f32_e32 v28, s45, v20
	v_mul_f32_e32 v29, s45, v21
	v_mul_f32_e32 v30, s45, v22
	v_mul_f32_e32 v31, s45, v23
	v_mfma_f32_32x32x16_f16 v[72:87], v[192:195], v[12:15], v[72:87]
	v_cmp_lt_i32_e64 s[60:61], 0, v108
	v_cmp_lt_i32_e64 s[62:63], 0, v109
	v_cmp_lt_i32_e64 s[64:65], 0, v110
	v_cmp_lt_i32_e64 s[66:67], 0, v111
	v_max_f32_e32 v24, v24, v28
	v_max_f32_e32 v25, v25, v29
	v_max_f32_e32 v26, v26, v30
	v_max_f32_e32 v27, v27, v31
	v_cndmask_b32_e64 v24, 0, v24, s[60:61]
	v_cndmask_b32_e64 v25, 0, v25, s[62:63]
	v_cndmask_b32_e64 v26, 0, v26, s[64:65]
	v_cndmask_b32_e64 v27, 0, v27, s[66:67]
	v_mfma_f32_32x32x16_f16 v[40:55], v[196:199], v[224:227], v[40:55]
	v_cvt_pkrtz_f16_f32 v34, v24, v25
	v_cvt_pkrtz_f16_f32 v35, v26, v27
	ds_write2_b64 v4, v[32:33], v[34:35] offset0:0 offset1:66
	v_mul_f32_e32 v24, s38, v16
	v_mul_f32_e32 v25, s38, v17
	v_mul_f32_e32 v26, s38, v18
	v_mul_f32_e32 v27, s38, v19
	v_mul_f32_e32 v28, s46, v20
	v_mul_f32_e32 v29, s46, v21
	v_mul_f32_e32 v30, s46, v22
	v_mul_f32_e32 v31, s46, v23
	v_mfma_f32_32x32x16_f16 v[56:71], v[196:199], v[228:231], v[56:71]
	v_cmp_lt_i32_e64 s[60:61], 0, v112
	v_cmp_lt_i32_e64 s[62:63], 0, v113
	v_cmp_lt_i32_e64 s[64:65], 0, v114
	v_cmp_lt_i32_e64 s[66:67], 0, v115
	v_max_f32_e32 v24, v24, v28
	v_max_f32_e32 v25, v25, v29
	v_max_f32_e32 v26, v26, v30
	v_max_f32_e32 v27, v27, v31
	v_cndmask_b32_e64 v24, 0, v24, s[60:61]
	v_cndmask_b32_e64 v25, 0, v25, s[62:63]
	v_cndmask_b32_e64 v26, 0, v26, s[64:65]
	v_cndmask_b32_e64 v27, 0, v27, s[66:67]
	v_cvt_pkrtz_f16_f32 v32, v24, v25
	v_cvt_pkrtz_f16_f32 v33, v26, v27
	v_mul_f32_e32 v24, s39, v16
	v_mul_f32_e32 v25, s39, v17
	v_mul_f32_e32 v26, s39, v18
	v_mul_f32_e32 v27, s39, v19
	v_mul_f32_e32 v28, s47, v20
	v_mul_f32_e32 v29, s47, v21
	v_mul_f32_e32 v30, s47, v22
	v_mul_f32_e32 v31, s47, v23
	v_mfma_f32_32x32x16_f16 v[72:87], v[196:199], v[12:15], v[72:87]
	v_cmp_lt_i32_e64 s[60:61], 0, v116
	v_cmp_lt_i32_e64 s[62:63], 0, v117
	v_cmp_lt_i32_e64 s[64:65], 0, v118
	v_cmp_lt_i32_e64 s[66:67], 0, v119
	v_max_f32_e32 v24, v24, v28
	v_max_f32_e32 v25, v25, v29
	v_max_f32_e32 v26, v26, v30
	v_max_f32_e32 v27, v27, v31
	v_cndmask_b32_e64 v24, 0, v24, s[60:61]
	v_cndmask_b32_e64 v25, 0, v25, s[62:63]
	v_cndmask_b32_e64 v26, 0, v26, s[64:65]
	v_cndmask_b32_e64 v27, 0, v27, s[66:67]
	v_cvt_pkrtz_f16_f32 v34, v24, v25
	v_cvt_pkrtz_f16_f32 v35, v26, v27
	ds_write2_b64 v4, v[32:33], v[34:35] offset0:132 offset1:198
	ds_write_b128 v9, v[152:155] offset:0
	ds_write_b128 v9, v[156:159] offset:1024
	ds_write_b128 v9, v[160:163] offset:2048
	ds_write_b128 v9, v[164:167] offset:3072
	s_add_u32 s3, s19, 7
	s_and_b32 s3, s3, 7
	s_lshl_b32 s3, s3, 10
	v_add_u32_e32 v11, s3, v10
	ds_read_b128 v[16:19], v11
	ds_read_b128 v[20:23], v11 offset:8192
	s_waitcnt lgkmcnt(0)
	s_barrier
	ds_read_b128 v[184:187], v7 offset:0
	ds_read_b128 v[200:203], v8 offset:0
	ds_read_b128 v[204:207], v8 offset:1024
	ds_read_b128 v[188:191], v7 offset:32
	ds_read_b128 v[208:211], v8 offset:2048
	ds_read_b128 v[212:215], v8 offset:3072
	ds_read_b128 v[192:195], v7 offset:64
	ds_read_b128 v[216:219], v8 offset:4096
	ds_read_b128 v[220:223], v8 offset:5120
	ds_read_b128 v[196:199], v7 offset:96
	ds_read_b128 v[224:227], v8 offset:6144
	ds_read_b128 v[228:231], v8 offset:7168
	s_waitcnt vmcnt(0)
	v_mul_f32_e32 v24, s32, v16
	v_mul_f32_e32 v25, s32, v17
	v_mul_f32_e32 v26, s32, v18
	v_mul_f32_e32 v27, s32, v19
	v_mul_f32_e32 v28, s40, v20
	v_mul_f32_e32 v29, s40, v21
	v_mul_f32_e32 v30, s40, v22
	v_mul_f32_e32 v31, s40, v23
	v_cmp_lt_i32_e64 s[60:61], 0, v120
	v_cmp_lt_i32_e64 s[62:63], 0, v121
	v_cmp_lt_i32_e64 s[64:65], 0, v122
	v_cmp_lt_i32_e64 s[66:67], 0, v123
	v_max_f32_e32 v24, v24, v28
	v_max_f32_e32 v25, v25, v29
	v_max_f32_e32 v26, v26, v30
	v_max_f32_e32 v27, v27, v31
	v_cndmask_b32_e64 v24, 0, v24, s[60:61]
	v_cndmask_b32_e64 v25, 0, v25, s[62:63]
	v_cndmask_b32_e64 v26, 0, v26, s[64:65]
	v_cndmask_b32_e64 v27, 0, v27, s[66:67]
	v_cvt_pkrtz_f16_f32 v32, v24, v25
	v_cvt_pkrtz_f16_f32 v33, v26, v27
	s_waitcnt lgkmcnt(0)
	v_mul_f32_e32 v24, s33, v16
	v_mul_f32_e32 v25, s33, v17
	v_mul_f32_e32 v26, s33, v18
	v_mul_f32_e32 v27, s33, v19
	v_mul_f32_e32 v28, s41, v20
	v_mul_f32_e32 v29, s41, v21
	v_mul_f32_e32 v30, s41, v22
	v_mul_f32_e32 v31, s41, v23
	v_mfma_f32_32x32x16_f16 v[40:55], v[184:187], v[200:203], v[40:55]
	v_cmp_lt_i32_e64 s[60:61], 0, v124
	v_cmp_lt_i32_e64 s[62:63], 0, v125
	v_cmp_lt_i32_e64 s[64:65], 0, v126
	v_cmp_lt_i32_e64 s[66:67], 0, v127
	v_max_f32_e32 v24, v24, v28
	v_max_f32_e32 v25, v25, v29
	v_max_f32_e32 v26, v26, v30
	v_max_f32_e32 v27, v27, v31
	v_cndmask_b32_e64 v24, 0, v24, s[60:61]
	v_cndmask_b32_e64 v25, 0, v25, s[62:63]
	v_cndmask_b32_e64 v26, 0, v26, s[64:65]
	v_cndmask_b32_e64 v27, 0, v27, s[66:67]
	v_mfma_f32_32x32x16_f16 v[56:71], v[184:187], v[204:207], v[56:71]
	v_cvt_pkrtz_f16_f32 v34, v24, v25
	v_cvt_pkrtz_f16_f32 v35, v26, v27
	ds_write2_b64 v5, v[32:33], v[34:35] offset0:0 offset1:66
	v_mul_f32_e32 v24, s34, v16
	v_mul_f32_e32 v25, s34, v17
	v_mul_f32_e32 v26, s34, v18
	v_mul_f32_e32 v27, s34, v19
	v_mul_f32_e32 v28, s42, v20
	v_mul_f32_e32 v29, s42, v21
	v_mul_f32_e32 v30, s42, v22
	v_mul_f32_e32 v31, s42, v23
	v_mfma_f32_32x32x16_f16 v[72:87], v[184:187], v[12:15], v[72:87]
	v_cmp_lt_i32_e64 s[60:61], 0, v128
	v_cmp_lt_i32_e64 s[62:63], 0, v129
	v_cmp_lt_i32_e64 s[64:65], 0, v130
	v_cmp_lt_i32_e64 s[66:67], 0, v131
	v_max_f32_e32 v24, v24, v28
	v_max_f32_e32 v25, v25, v29
	v_max_f32_e32 v26, v26, v30
	v_max_f32_e32 v27, v27, v31
	v_cndmask_b32_e64 v24, 0, v24, s[60:61]
	v_cndmask_b32_e64 v25, 0, v25, s[62:63]
	v_cndmask_b32_e64 v26, 0, v26, s[64:65]
	v_cndmask_b32_e64 v27, 0, v27, s[66:67]
	v_mfma_f32_32x32x16_f16 v[40:55], v[188:191], v[208:211], v[40:55]
	v_cvt_pkrtz_f16_f32 v32, v24, v25
	v_cvt_pkrtz_f16_f32 v33, v26, v27
	v_mul_f32_e32 v24, s35, v16
	v_mul_f32_e32 v25, s35, v17
	v_mul_f32_e32 v26, s35, v18
	v_mul_f32_e32 v27, s35, v19
	v_mul_f32_e32 v28, s43, v20
	v_mul_f32_e32 v29, s43, v21
	v_mul_f32_e32 v30, s43, v22
	v_mul_f32_e32 v31, s43, v23
	v_mfma_f32_32x32x16_f16 v[56:71], v[188:191], v[212:215], v[56:71]
	v_cmp_lt_i32_e64 s[60:61], 0, v132
	v_cmp_lt_i32_e64 s[62:63], 0, v133
	v_cmp_lt_i32_e64 s[64:65], 0, v134
	v_cmp_lt_i32_e64 s[66:67], 0, v135
	v_max_f32_e32 v24, v24, v28
	v_max_f32_e32 v25, v25, v29
	v_max_f32_e32 v26, v26, v30
	v_max_f32_e32 v27, v27, v31
	v_cndmask_b32_e64 v24, 0, v24, s[60:61]
	v_cndmask_b32_e64 v25, 0, v25, s[62:63]
	v_cndmask_b32_e64 v26, 0, v26, s[64:65]
	v_cndmask_b32_e64 v27, 0, v27, s[66:67]
	v_mfma_f32_32x32x16_f16 v[72:87], v[188:191], v[12:15], v[72:87]
	v_cvt_pkrtz_f16_f32 v34, v24, v25
	v_cvt_pkrtz_f16_f32 v35, v26, v27
	ds_write2_b64 v5, v[32:33], v[34:35] offset0:132 offset1:198
	v_mul_f32_e32 v24, s36, v16
	v_mul_f32_e32 v25, s36, v17
	v_mul_f32_e32 v26, s36, v18
	v_mul_f32_e32 v27, s36, v19
	v_mul_f32_e32 v28, s44, v20
	v_mul_f32_e32 v29, s44, v21
	v_mul_f32_e32 v30, s44, v22
	v_mul_f32_e32 v31, s44, v23
	v_mfma_f32_32x32x16_f16 v[40:55], v[192:195], v[216:219], v[40:55]
	v_cmp_lt_i32_e64 s[60:61], 0, v136
	v_cmp_lt_i32_e64 s[62:63], 0, v137
	v_cmp_lt_i32_e64 s[64:65], 0, v138
	v_cmp_lt_i32_e64 s[66:67], 0, v139
	v_max_f32_e32 v24, v24, v28
	v_max_f32_e32 v25, v25, v29
	v_max_f32_e32 v26, v26, v30
	v_max_f32_e32 v27, v27, v31
	v_cndmask_b32_e64 v24, 0, v24, s[60:61]
	v_cndmask_b32_e64 v25, 0, v25, s[62:63]
	v_cndmask_b32_e64 v26, 0, v26, s[64:65]
	v_cndmask_b32_e64 v27, 0, v27, s[66:67]
	v_mfma_f32_32x32x16_f16 v[56:71], v[192:195], v[220:223], v[56:71]
	v_cvt_pkrtz_f16_f32 v32, v24, v25
	v_cvt_pkrtz_f16_f32 v33, v26, v27
	v_mul_f32_e32 v24, s37, v16
	v_mul_f32_e32 v25, s37, v17
	v_mul_f32_e32 v26, s37, v18
	v_mul_f32_e32 v27, s37, v19
	v_mul_f32_e32 v28, s45, v20
	v_mul_f32_e32 v29, s45, v21
	v_mul_f32_e32 v30, s45, v22
	v_mul_f32_e32 v31, s45, v23
	v_mfma_f32_32x32x16_f16 v[72:87], v[192:195], v[12:15], v[72:87]
	v_cmp_lt_i32_e64 s[60:61], 0, v140
	v_cmp_lt_i32_e64 s[62:63], 0, v141
	v_cmp_lt_i32_e64 s[64:65], 0, v142
	v_cmp_lt_i32_e64 s[66:67], 0, v143
	v_max_f32_e32 v24, v24, v28
	v_max_f32_e32 v25, v25, v29
	v_max_f32_e32 v26, v26, v30
	v_max_f32_e32 v27, v27, v31
	v_cndmask_b32_e64 v24, 0, v24, s[60:61]
	v_cndmask_b32_e64 v25, 0, v25, s[62:63]
	v_cndmask_b32_e64 v26, 0, v26, s[64:65]
	v_cndmask_b32_e64 v27, 0, v27, s[66:67]
	v_mfma_f32_32x32x16_f16 v[40:55], v[196:199], v[224:227], v[40:55]
	v_cvt_pkrtz_f16_f32 v34, v24, v25
	v_cvt_pkrtz_f16_f32 v35, v26, v27
	ds_write2_b64 v6, v[32:33], v[34:35] offset0:0 offset1:66
	v_mul_f32_e32 v24, s38, v16
	v_mul_f32_e32 v25, s38, v17
	v_mul_f32_e32 v26, s38, v18
	v_mul_f32_e32 v27, s38, v19
	v_mul_f32_e32 v28, s46, v20
	v_mul_f32_e32 v29, s46, v21
	v_mul_f32_e32 v30, s46, v22
	v_mul_f32_e32 v31, s46, v23
	v_mfma_f32_32x32x16_f16 v[56:71], v[196:199], v[228:231], v[56:71]
	v_cmp_lt_i32_e64 s[60:61], 0, v144
	v_cmp_lt_i32_e64 s[62:63], 0, v145
	v_cmp_lt_i32_e64 s[64:65], 0, v146
	v_cmp_lt_i32_e64 s[66:67], 0, v147
	v_max_f32_e32 v24, v24, v28
	v_max_f32_e32 v25, v25, v29
	v_max_f32_e32 v26, v26, v30
	v_max_f32_e32 v27, v27, v31
	v_cndmask_b32_e64 v24, 0, v24, s[60:61]
	v_cndmask_b32_e64 v25, 0, v25, s[62:63]
	v_cndmask_b32_e64 v26, 0, v26, s[64:65]
	v_cndmask_b32_e64 v27, 0, v27, s[66:67]
	v_cvt_pkrtz_f16_f32 v32, v24, v25
	v_cvt_pkrtz_f16_f32 v33, v26, v27
	v_mul_f32_e32 v24, s39, v16
	v_mul_f32_e32 v25, s39, v17
	v_mul_f32_e32 v26, s39, v18
	v_mul_f32_e32 v27, s39, v19
	v_mul_f32_e32 v28, s47, v20
	v_mul_f32_e32 v29, s47, v21
	v_mul_f32_e32 v30, s47, v22
	v_mul_f32_e32 v31, s47, v23
	v_mfma_f32_32x32x16_f16 v[72:87], v[196:199], v[12:15], v[72:87]
	v_cmp_lt_i32_e64 s[60:61], 0, v148
	v_cmp_lt_i32_e64 s[62:63], 0, v149
	v_cmp_lt_i32_e64 s[64:65], 0, v150
	v_cmp_lt_i32_e64 s[66:67], 0, v151
	v_max_f32_e32 v24, v24, v28
	v_max_f32_e32 v25, v25, v29
	v_max_f32_e32 v26, v26, v30
	v_max_f32_e32 v27, v27, v31
	v_cndmask_b32_e64 v24, 0, v24, s[60:61]
	v_cndmask_b32_e64 v25, 0, v25, s[62:63]
	v_cndmask_b32_e64 v26, 0, v26, s[64:65]
	v_cndmask_b32_e64 v27, 0, v27, s[66:67]
	v_cvt_pkrtz_f16_f32 v34, v24, v25
	v_cvt_pkrtz_f16_f32 v35, v26, v27
	ds_write2_b64 v6, v[32:33], v[34:35] offset0:132 offset1:198
	ds_write_b128 v9, v[168:171] offset:32768
	ds_write_b128 v9, v[172:175] offset:33792
	ds_write_b128 v9, v[176:179] offset:34816
	ds_write_b128 v9, v[180:183] offset:35840
	s_waitcnt lgkmcnt(0)
	s_barrier
	ds_read_b128 v[184:187], v7 offset:33792
	ds_read_b128 v[200:203], v8 offset:32768
	ds_read_b128 v[204:207], v8 offset:33792
	ds_read_b128 v[188:191], v7 offset:33824
	ds_read_b128 v[208:211], v8 offset:34816
	ds_read_b128 v[212:215], v8 offset:35840
	ds_read_b128 v[192:195], v7 offset:33856
	ds_read_b128 v[216:219], v8 offset:36864
	ds_read_b128 v[220:223], v8 offset:37888
	ds_read_b128 v[196:199], v7 offset:33888
	ds_read_b128 v[224:227], v8 offset:38912
	ds_read_b128 v[228:231], v8 offset:39936
	s_waitcnt lgkmcnt(0)
	v_mfma_f32_32x32x16_f16 v[40:55], v[184:187], v[200:203], v[40:55]
	v_mfma_f32_32x32x16_f16 v[56:71], v[184:187], v[204:207], v[56:71]
	v_mfma_f32_32x32x16_f16 v[72:87], v[184:187], v[12:15], v[72:87]
	v_mfma_f32_32x32x16_f16 v[40:55], v[188:191], v[208:211], v[40:55]
	v_mfma_f32_32x32x16_f16 v[56:71], v[188:191], v[212:215], v[56:71]
	v_mfma_f32_32x32x16_f16 v[72:87], v[188:191], v[12:15], v[72:87]
	v_mfma_f32_32x32x16_f16 v[40:55], v[192:195], v[216:219], v[40:55]
	v_mfma_f32_32x32x16_f16 v[56:71], v[192:195], v[220:223], v[56:71]
	v_mfma_f32_32x32x16_f16 v[72:87], v[192:195], v[12:15], v[72:87]
	v_mfma_f32_32x32x16_f16 v[40:55], v[196:199], v[224:227], v[40:55]
	v_mfma_f32_32x32x16_f16 v[56:71], v[196:199], v[228:231], v[56:71]
	v_mfma_f32_32x32x16_f16 v[72:87], v[196:199], v[12:15], v[72:87]
	s_nop 15
	s_barrier
	s_mul_i32 s3, s20, 0xc000
	s_mul_i32 s57, s21, 0xc00
	s_add_u32 s3, s3, s57
	v_add_u32_e32 v36, s3, v1
	ds_write_b128 v36, v[40:43] offset:0
	ds_write_b128 v36, v[56:59] offset:1024
	ds_write_b128 v36, v[72:75] offset:2048
	ds_write_b128 v36, v[44:47] offset:12288
	ds_write_b128 v36, v[60:63] offset:13312
	ds_write_b128 v36, v[76:79] offset:14336
	ds_write_b128 v36, v[48:51] offset:24576
	ds_write_b128 v36, v[64:67] offset:25600
	ds_write_b128 v36, v[80:83] offset:26624
	ds_write_b128 v36, v[52:55] offset:36864
	ds_write_b128 v36, v[68:71] offset:37888
	ds_write_b128 v36, v[84:87] offset:38912
	s_waitcnt lgkmcnt(0)
	s_barrier
	s_mul_i32 s3, s16, 0x3000
	v_add_u32_e32 v36, s3, v1
	ds_read_b128 v[40:43], v36 offset:0
	ds_read_b128 v[44:47], v36 offset:1024
	ds_read_b128 v[48:51], v36 offset:2048
	ds_read_b128 v[52:55], v36 offset:3072
	ds_read_b128 v[56:59], v36 offset:4096
	ds_read_b128 v[60:63], v36 offset:5120
	ds_read_b128 v[64:67], v36 offset:6144
	ds_read_b128 v[68:71], v36 offset:7168
	ds_read_b128 v[72:75], v36 offset:8192
	ds_read_b128 v[76:79], v36 offset:9216
	ds_read_b128 v[80:83], v36 offset:10240
	ds_read_b128 v[84:87], v36 offset:11264
	s_waitcnt lgkmcnt(0)
	v_add_f32_e32 v40, v40, v52
	v_add_f32_e32 v41, v41, v53
	v_add_f32_e32 v42, v42, v54
	v_add_f32_e32 v43, v43, v55
	v_add_f32_e32 v44, v44, v56
	v_add_f32_e32 v45, v45, v57
	v_add_f32_e32 v46, v46, v58
	v_add_f32_e32 v47, v47, v59
	v_add_f32_e32 v48, v48, v60
	v_add_f32_e32 v49, v49, v61
	v_add_f32_e32 v50, v50, v62
	v_add_f32_e32 v51, v51, v63
	v_add_f32_e32 v40, v40, v64
	v_add_f32_e32 v41, v41, v65
	v_add_f32_e32 v42, v42, v66
	v_add_f32_e32 v43, v43, v67
	v_add_f32_e32 v44, v44, v68
	v_add_f32_e32 v45, v45, v69
	v_add_f32_e32 v46, v46, v70
	v_add_f32_e32 v47, v47, v71
	v_add_f32_e32 v48, v48, v72
	v_add_f32_e32 v49, v49, v73
	v_add_f32_e32 v50, v50, v74
	v_add_f32_e32 v51, v51, v75
	v_add_f32_e32 v40, v40, v76
	v_add_f32_e32 v41, v41, v77
	v_add_f32_e32 v42, v42, v78
	v_add_f32_e32 v43, v43, v79
	v_add_f32_e32 v44, v44, v80
	v_add_f32_e32 v45, v45, v81
	v_add_f32_e32 v46, v46, v82
	v_add_f32_e32 v47, v47, v83
	v_add_f32_e32 v48, v48, v84
	v_add_f32_e32 v49, v49, v85
	v_add_f32_e32 v50, v50, v86
	v_add_f32_e32 v51, v51, v87
	v_cmp_eq_f32_e64 s[60:61], 0, v48
	v_cmp_eq_f32_e64 s[62:63], 0, v49
	v_cmp_eq_f32_e64 s[64:65], 0, v50
	v_cmp_eq_f32_e64 s[66:67], 0, v51
	s_nop 3
	s_or_b64 s[60:61], s[60:61], s[62:63]
	s_or_b64 s[64:65], s[64:65], s[66:67]
	s_or_b64 s[60:61], s[60:61], s[64:65]
	s_cmp_eq_u64 s[60:61], 0
	s_cbranch_scc1 .Lgm_no_fallback
	v_and_b32_e32 v101, 31, v2
	v_lshlrev_b32_e32 v101, 4, v101
	v_mov_b32_e32 v88, 0
	v_mov_b32_e32 v89, 0
	s_mov_b32 s3, 0
